# speedup vs baseline: 1.0116x; 1.0005x over previous
.LBB3_35:
	s_andn2_b64 vcc, exec, s[2:3]
	s_cbranch_vccnz .LBB3_39
	s_waitcnt vmcnt(4)
	v_ashrrev_i32_e32 v81, 31, v80
	v_lshl_add_u64 v[2:3], v[80:81], 3, s[20:21]
	v_add_co_u32_e32 v2, vcc, 0x48000, v2
	s_movk_i32 s8, 0x620
	s_nop 0
	v_addc_co_u32_e32 v3, vcc, 0, v3, vcc
	global_load_dwordx2 v[82:83], v[2:3], off
	v_and_b32_e32 v2, 0x70, v7
	v_bitop3_b32 v2, v0, v2, 48 bitop3:0x6c
	s_waitcnt vmcnt(4)
	v_mad_u64_u32 v[64:65], s[6:7], v9, s8, v[2:3]
	v_lshrrev_b32_e32 v3, 4, v92
	v_bitop3_b32 v3, v3, v0, 4 bitop3:0x36
	v_lshlrev_b32_e32 v3, 4, v3
	v_and_b32_e32 v4, 0x70, v3
	s_waitcnt vmcnt(3)
	v_mad_u64_u32 v[66:67], s[6:7], v8, s8, v[4:5]
	s_waitcnt vmcnt(2)
	v_mad_u64_u32 v[68:69], s[6:7], v6, s8, v[2:3]
	s_waitcnt vmcnt(1)
	v_mad_u64_u32 v[70:71], s[6:7], v1, s8, v[4:5]
	v_lshrrev_b32_e32 v85, 5, v92
	v_bfe_u32 v2, v0, 1, 3
	s_mov_b64 s[6:7], 0x1800
	s_add_u32 s4, s20, 0x4000000
	v_bitop3_b32 v32, v85, v2, 2 bitop3:0x36
	v_bitop3_b32 v33, v85, v2, 4 bitop3:0x36
	v_bitop3_b32 v34, v85, v2, 6 bitop3:0x36
	v_lshl_add_u64 v[2:3], v[86:87], 0, s[6:7]
	s_addc_u32 s5, s21, 0
	s_lshl_b32 s2, s27, 12
	s_addk_i32 s2, 0x6000
	v_lshrrev_b32_e32 v1, 1, v0
	v_or_b32_e32 v81, s2, v84
	v_lshlrev_b32_e32 v0, 7, v0
	v_and_b32_e32 v8, 0xf80, v0
	v_lshlrev_b32_e32 v9, 4, v32
	v_bitop3_b32 v1, v85, v1, 7 bitop3:0x78
	v_or3_b32 v96, s2, v9, v8
	v_lshlrev_b32_e32 v9, 4, v33
	v_lshlrev_b32_e32 v1, 4, v1
	v_or3_b32 v97, s2, v9, v8
	v_lshlrev_b32_e32 v9, 4, v34
	v_or3_b32 v95, s2, v1, v8
	v_or3_b32 v94, s2, v9, v8
	v_add_u32_e32 v98, 0x103c0, v84
	global_load_dwordx4 v[116:119], v64, s[4:5] offset:0
	global_load_dwordx4 v[120:123], v66, s[4:5] offset:0
	global_load_dwordx4 v[124:127], v68, s[4:5] offset:0
	global_load_dwordx4 v[128:131], v70, s[4:5] offset:0
	global_load_dwordx4 v[132:135], v64, s[4:5] offset:128
	global_load_dwordx4 v[136:139], v66, s[4:5] offset:128
	global_load_dwordx4 v[140:143], v68, s[4:5] offset:128
	global_load_dwordx4 v[144:147], v70, s[4:5] offset:128
	global_load_dwordx4 v[148:151], v64, s[4:5] offset:256
	global_load_dwordx4 v[152:155], v66, s[4:5] offset:256
	global_load_dwordx4 v[156:159], v68, s[4:5] offset:256
	global_load_dwordx4 v[72:75], v70, s[4:5] offset:256
	s_add_u32 m0, s46, 0x0
	s_nop 0
	global_load_lds_dwordx4 v76, s[40:41]
	s_add_u32 m0, s47, 0x0
	s_nop 0
	global_load_lds_dwordx4 v77, s[42:43]
	s_add_u32 m0, s48, 0x0
	s_nop 0
	global_load_lds_dwordx4 v78, s[44:45]
	s_add_u32 m0, s46, 0x3000
	s_add_u32 s40, s40, 0x1800
	s_addc_u32 s41, s41, 0
	global_load_lds_dwordx4 v76, s[40:41]
	s_add_u32 m0, s47, 0x3000
	s_add_u32 s42, s42, 0x1800
	s_addc_u32 s43, s43, 0
	global_load_lds_dwordx4 v77, s[42:43]
	s_add_u32 m0, s48, 0x3000
	s_add_u32 s44, s44, 0x1800
	s_addc_u32 s45, s45, 0
	global_load_lds_dwordx4 v78, s[44:45]
	s_add_u32 m0, s46, 0xd3c0
	s_add_u32 s40, s40, 0x1800
	s_addc_u32 s41, s41, 0
	global_load_lds_dwordx4 v76, s[40:41]
	s_add_u32 m0, s47, 0xd3c0
	s_add_u32 s42, s42, 0x1800
	s_addc_u32 s43, s43, 0
	global_load_lds_dwordx4 v77, s[42:43]
	s_add_u32 m0, s48, 0xd3c0
	s_add_u32 s44, s44, 0x1800
	s_addc_u32 s45, s45, 0
	global_load_lds_dwordx4 v78, s[44:45]
	s_add_u32 m0, s46, 0x103c0
	s_add_u32 s40, s40, 0x1800
	s_addc_u32 s41, s41, 0
	global_load_lds_dwordx4 v76, s[40:41]
	s_add_u32 m0, s47, 0x103c0
	s_add_u32 s42, s42, 0x1800
	s_addc_u32 s43, s43, 0
	global_load_lds_dwordx4 v77, s[42:43]
	s_add_u32 m0, s48, 0x103c0
	s_add_u32 s44, s44, 0x1800
	s_addc_u32 s45, s45, 0
	global_load_lds_dwordx4 v78, s[44:45]
	s_waitcnt vmcnt(20)
	ds_write_b128 v81, v[116:119]
	ds_write_b128 v81, v[120:123] offset:1024
	ds_write_b128 v81, v[124:127] offset:2048
	ds_write_b128 v81, v[128:131] offset:3072
	ds_read_b128 v[52:55], v95
	ds_read_b128 v[56:59], v96
	ds_read_b128 v[60:63], v97
	ds_read_b128 v[0:3], v94
	global_load_dwordx4 v[116:119], v64, s[4:5] offset:384
	global_load_dwordx4 v[120:123], v66, s[4:5] offset:384
	global_load_dwordx4 v[124:127], v68, s[4:5] offset:384
	global_load_dwordx4 v[128:131], v70, s[4:5] offset:384
	s_waitcnt vmcnt(13)
	s_waitcnt lgkmcnt(0)
	s_barrier
	ds_read_b128 v[4:7], v84 offset:0
	ds_read_b128 v[8:11], v84 offset:1024
	ds_read_b128 v[12:15], v84 offset:2048
	ds_read_b128 v[16:19], v84 offset:3072
	ds_read_b128 v[20:23], v84 offset:4096
	ds_read_b128 v[24:27], v84 offset:5120
	ds_read_b128 v[28:31], v84 offset:6144
	ds_read_b128 v[32:35], v84 offset:7168
	ds_read_b128 v[36:39], v84 offset:8192
	ds_read_b128 v[40:43], v84 offset:9216
	ds_read_b128 v[44:47], v84 offset:10240
	ds_read_b128 v[48:51], v84 offset:11264
	s_waitcnt lgkmcnt(6)
	v_mfma_f32_32x32x16_f16 a[80:95], v[4:7], v[52:55], 0
	v_mfma_f32_32x32x16_f16 a[64:79], v[8:11], v[52:55], 0
	v_mfma_f32_32x32x16_f16 a[48:63], v[12:15], v[52:55], 0
	s_waitcnt vmcnt(10)
	s_waitcnt lgkmcnt(0)
	s_barrier
	ds_read_b128 v[4:7], v84 offset:12288
	ds_read_b128 v[8:11], v84 offset:13312
	ds_read_b128 v[12:15], v84 offset:14336
	s_nop 0
	v_mfma_f32_32x32x16_f16 a[32:47], v[16:19], v[52:55], 0
	ds_read_b128 v[16:19], v84 offset:15360
	v_mfma_f32_32x32x16_f16 a[16:31], v[20:23], v[52:55], 0
	ds_read_b128 v[20:23], v84 offset:16384
	v_mfma_f32_32x32x16_f16 a[0:15], v[24:27], v[52:55], 0
	ds_read_b128 v[24:27], v84 offset:17408
	v_mfma_f32_32x32x16_f16 a[80:95], v[28:31], v[56:59], a[80:95]
	s_add_u32 m0, s46, 0x0
	s_add_u32 s40, s40, 0x1800
	s_addc_u32 s41, s41, 0
	global_load_lds_dwordx4 v76, s[40:41]
	ds_read_b128 v[28:31], v84 offset:18432
	v_mfma_f32_32x32x16_f16 a[64:79], v[32:35], v[56:59], a[64:79]
	ds_read_b128 v[32:35], v84 offset:19456
	v_mfma_f32_32x32x16_f16 a[48:63], v[36:39], v[56:59], a[48:63]
	s_add_u32 m0, s47, 0x0
	s_add_u32 s42, s42, 0x1800
	s_addc_u32 s43, s43, 0
	global_load_lds_dwordx4 v77, s[42:43]
	ds_read_b128 v[36:39], v84 offset:20480
	v_mfma_f32_32x32x16_f16 a[32:47], v[40:43], v[56:59], a[32:47]
	ds_read_b128 v[40:43], v84 offset:21504
	v_mfma_f32_32x32x16_f16 a[16:31], v[44:47], v[56:59], a[16:31]
	s_add_u32 m0, s48, 0x0
	s_add_u32 s44, s44, 0x1800
	s_addc_u32 s45, s45, 0
	global_load_lds_dwordx4 v78, s[44:45]
	ds_read_b128 v[44:47], v84 offset:22528
	v_mfma_f32_32x32x16_f16 a[0:15], v[48:51], v[56:59], a[0:15]
	ds_read_b128 v[48:51], v84 offset:23552
	s_waitcnt lgkmcnt(6)
	s_nop 0
	v_mfma_f32_32x32x16_f16 a[80:95], v[4:7], v[60:63], a[80:95]
	s_waitcnt vmcnt(23)
	ds_write_b128 v81, v[132:135]
	ds_write_b128 v81, v[136:139] offset:1024
	s_nop 0
	v_mfma_f32_32x32x16_f16 a[64:79], v[8:11], v[60:63], a[64:79]
	ds_write_b128 v81, v[140:143] offset:2048
	ds_write_b128 v81, v[144:147] offset:3072
	v_mfma_f32_32x32x16_f16 a[48:63], v[12:15], v[60:63], a[48:63]
	ds_read_b128 v[100:103], v95
	ds_read_b128 v[104:107], v96
	ds_read_b128 v[108:111], v97
	ds_read_b128 v[112:115], v94
	s_waitcnt vmcnt(10)
	s_waitcnt lgkmcnt(8)
	s_barrier
	ds_read_b128 v[4:7], v84 offset:54208
	ds_read_b128 v[8:11], v84 offset:55232
	ds_read_b128 v[12:15], v84 offset:56256
	s_nop 0
	v_mfma_f32_32x32x16_f16 a[32:47], v[16:19], v[60:63], a[32:47]
	ds_read_b128 v[16:19], v84 offset:57280
	v_mfma_f32_32x32x16_f16 a[16:31], v[20:23], v[60:63], a[16:31]
	ds_read_b128 v[20:23], v84 offset:58304
	v_mfma_f32_32x32x16_f16 a[0:15], v[24:27], v[60:63], a[0:15]
	ds_read_b128 v[24:27], v84 offset:59328
	s_waitcnt lgkmcnt(6)
	s_nop 0
	v_mfma_f32_32x32x16_f16 a[80:95], v[28:31], v[0:3], a[80:95]
	s_add_u32 m0, s46, 0x3000
	s_add_u32 s40, s40, 0x1800
	s_addc_u32 s41, s41, 0
	global_load_lds_dwordx4 v76, s[40:41]
	ds_read_b128 v[28:31], v84 offset:60352
	s_nop 0
	v_mfma_f32_32x32x16_f16 a[64:79], v[32:35], v[0:3], a[64:79]
	global_load_dwordx4 v[132:135], v64, s[4:5] offset:512
	global_load_dwordx4 v[136:139], v66, s[4:5] offset:512
	ds_read_b128 v[32:35], v84 offset:61376
	v_mfma_f32_32x32x16_f16 a[48:63], v[36:39], v[0:3], a[48:63]
	s_add_u32 m0, s47, 0x3000
	s_add_u32 s42, s42, 0x1800
	s_addc_u32 s43, s43, 0
	global_load_lds_dwordx4 v77, s[42:43]
	ds_read_b128 v[36:39], v84 offset:62400
	s_nop 0
	v_mfma_f32_32x32x16_f16 a[32:47], v[40:43], v[0:3], a[32:47]
	global_load_dwordx4 v[140:143], v68, s[4:5] offset:512
	global_load_dwordx4 v[144:147], v70, s[4:5] offset:512
	ds_read_b128 v[40:43], v84 offset:63424
	v_mfma_f32_32x32x16_f16 a[16:31], v[44:47], v[0:3], a[16:31]
	s_add_u32 m0, s48, 0x3000
	s_add_u32 s44, s44, 0x1800
	s_addc_u32 s45, s45, 0
	global_load_lds_dwordx4 v78, s[44:45]
	ds_read_b128 v[44:47], v84 offset:64448
	s_nop 0
	v_mfma_f32_32x32x16_f16 a[0:15], v[48:51], v[0:3], a[0:15]
	ds_read_b128 v[48:51], v84 offset:65472
	s_waitcnt lgkmcnt(6)
	s_nop 0
	v_mfma_f32_32x32x16_f16 a[80:95], v[4:7], v[100:103], a[80:95]
	v_mfma_f32_32x32x16_f16 a[64:79], v[8:11], v[100:103], a[64:79]
	v_mfma_f32_32x32x16_f16 a[48:63], v[12:15], v[100:103], a[48:63]
	s_waitcnt vmcnt(14)
	s_waitcnt lgkmcnt(0)
	s_barrier
	ds_read_b128 v[4:7], v98
	ds_read_b128 v[8:11], v98 offset:1024
	ds_read_b128 v[12:15], v98 offset:2048
	s_nop 0
	v_mfma_f32_32x32x16_f16 a[32:47], v[16:19], v[100:103], a[32:47]
	ds_read_b128 v[16:19], v98 offset:3072
	v_mfma_f32_32x32x16_f16 a[16:31], v[20:23], v[100:103], a[16:31]
	ds_read_b128 v[20:23], v98 offset:4096
	v_mfma_f32_32x32x16_f16 a[0:15], v[24:27], v[100:103], a[0:15]
	ds_read_b128 v[24:27], v98 offset:5120
	v_mfma_f32_32x32x16_f16 a[80:95], v[28:31], v[104:107], a[80:95]
	s_add_u32 m0, s46, 0xd3c0
	s_add_u32 s40, s40, 0x1800
	s_addc_u32 s41, s41, 0
	global_load_lds_dwordx4 v76, s[40:41]
	ds_read_b128 v[28:31], v98 offset:6144
	s_nop 0
	v_mfma_f32_32x32x16_f16 a[64:79], v[32:35], v[104:107], a[64:79]
	ds_read_b128 v[32:35], v98 offset:7168
	v_mfma_f32_32x32x16_f16 a[48:63], v[36:39], v[104:107], a[48:63]
	s_add_u32 m0, s47, 0xd3c0
	s_add_u32 s42, s42, 0x1800
	s_addc_u32 s43, s43, 0
	global_load_lds_dwordx4 v77, s[42:43]
	ds_read_b128 v[36:39], v98 offset:8192
	s_nop 0
	v_mfma_f32_32x32x16_f16 a[32:47], v[40:43], v[104:107], a[32:47]
	ds_read_b128 v[40:43], v98 offset:9216
	v_mfma_f32_32x32x16_f16 a[16:31], v[44:47], v[104:107], a[16:31]
	s_add_u32 m0, s48, 0xd3c0
	s_add_u32 s44, s44, 0x1800
	s_addc_u32 s45, s45, 0
	global_load_lds_dwordx4 v78, s[44:45]
	ds_read_b128 v[44:47], v98 offset:10240
	s_nop 0
	v_mfma_f32_32x32x16_f16 a[0:15], v[48:51], v[104:107], a[0:15]
	ds_read_b128 v[48:51], v98 offset:11264
	s_waitcnt lgkmcnt(6)
	s_nop 0
	v_mfma_f32_32x32x16_f16 a[80:95], v[4:7], v[108:111], a[80:95]
	s_waitcnt vmcnt(29)
	ds_write_b128 v81, v[148:151]
	ds_write_b128 v81, v[152:155] offset:1024
	s_nop 0
	v_mfma_f32_32x32x16_f16 a[64:79], v[8:11], v[108:111], a[64:79]
	ds_write_b128 v81, v[156:159] offset:2048
	ds_write_b128 v81, v[72:75] offset:3072
	v_mfma_f32_32x32x16_f16 a[48:63], v[12:15], v[108:111], a[48:63]
	ds_read_b128 v[52:55], v95
	ds_read_b128 v[56:59], v96
	ds_read_b128 v[60:63], v97
	ds_read_b128 v[0:3], v94
	s_waitcnt vmcnt(10)
	s_waitcnt lgkmcnt(8)
	s_barrier
	ds_read_b128 v[4:7], v84 offset:0
	ds_read_b128 v[8:11], v84 offset:1024
	ds_read_b128 v[12:15], v84 offset:2048
	s_nop 0
	v_mfma_f32_32x32x16_f16 a[32:47], v[16:19], v[108:111], a[32:47]
	ds_read_b128 v[16:19], v84 offset:3072
	v_mfma_f32_32x32x16_f16 a[16:31], v[20:23], v[108:111], a[16:31]
	ds_read_b128 v[20:23], v84 offset:4096
	v_mfma_f32_32x32x16_f16 a[0:15], v[24:27], v[108:111], a[0:15]
	ds_read_b128 v[24:27], v84 offset:5120
	s_waitcnt lgkmcnt(6)
	s_nop 0
	v_mfma_f32_32x32x16_f16 a[80:95], v[28:31], v[112:115], a[80:95]
	s_add_u32 m0, s46, 0x103c0
	s_add_u32 s40, s40, 0x1800
	s_addc_u32 s41, s41, 0
	global_load_lds_dwordx4 v76, s[40:41]
	ds_read_b128 v[28:31], v84 offset:6144
	s_nop 0
	v_mfma_f32_32x32x16_f16 a[64:79], v[32:35], v[112:115], a[64:79]
	global_load_dwordx4 v[148:151], v64, s[4:5] offset:640
	global_load_dwordx4 v[152:155], v66, s[4:5] offset:640
	ds_read_b128 v[32:35], v84 offset:7168
	v_mfma_f32_32x32x16_f16 a[48:63], v[36:39], v[112:115], a[48:63]
	s_add_u32 m0, s47, 0x103c0
	s_add_u32 s42, s42, 0x1800
	s_addc_u32 s43, s43, 0
	global_load_lds_dwordx4 v77, s[42:43]
	ds_read_b128 v[36:39], v84 offset:8192
	s_nop 0
	v_mfma_f32_32x32x16_f16 a[32:47], v[40:43], v[112:115], a[32:47]
	global_load_dwordx4 v[156:159], v68, s[4:5] offset:640
	global_load_dwordx4 v[72:75], v70, s[4:5] offset:640
	ds_read_b128 v[40:43], v84 offset:9216
	v_mfma_f32_32x32x16_f16 a[16:31], v[44:47], v[112:115], a[16:31]
	s_add_u32 m0, s48, 0x103c0
	s_add_u32 s44, s44, 0x1800
	s_addc_u32 s45, s45, 0
	global_load_lds_dwordx4 v78, s[44:45]
	ds_read_b128 v[44:47], v84 offset:10240
	s_nop 0
	v_mfma_f32_32x32x16_f16 a[0:15], v[48:51], v[112:115], a[0:15]
	ds_read_b128 v[48:51], v84 offset:11264
	s_waitcnt lgkmcnt(6)
	s_nop 0
	v_mfma_f32_32x32x16_f16 a[80:95], v[4:7], v[52:55], a[80:95]
	v_mfma_f32_32x32x16_f16 a[64:79], v[8:11], v[52:55], a[64:79]
	v_mfma_f32_32x32x16_f16 a[48:63], v[12:15], v[52:55], a[48:63]
	s_waitcnt vmcnt(10)
	s_waitcnt lgkmcnt(0)
	s_barrier
	ds_read_b128 v[4:7], v84 offset:12288
	ds_read_b128 v[8:11], v84 offset:13312
	ds_read_b128 v[12:15], v84 offset:14336
	s_nop 0
	v_mfma_f32_32x32x16_f16 a[32:47], v[16:19], v[52:55], a[32:47]
	ds_read_b128 v[16:19], v84 offset:15360
	v_mfma_f32_32x32x16_f16 a[16:31], v[20:23], v[52:55], a[16:31]
	ds_read_b128 v[20:23], v84 offset:16384
	v_mfma_f32_32x32x16_f16 a[0:15], v[24:27], v[52:55], a[0:15]
	ds_read_b128 v[24:27], v84 offset:17408
	v_mfma_f32_32x32x16_f16 a[80:95], v[28:31], v[56:59], a[80:95]
	s_add_u32 m0, s46, 0x0
	s_add_u32 s40, s40, 0x1800
	s_addc_u32 s41, s41, 0
	global_load_lds_dwordx4 v76, s[40:41]
	ds_read_b128 v[28:31], v84 offset:18432
	v_mfma_f32_32x32x16_f16 a[64:79], v[32:35], v[56:59], a[64:79]
	ds_read_b128 v[32:35], v84 offset:19456
	v_mfma_f32_32x32x16_f16 a[48:63], v[36:39], v[56:59], a[48:63]
	s_add_u32 m0, s47, 0x0
	s_add_u32 s42, s42, 0x1800
	s_addc_u32 s43, s43, 0
	global_load_lds_dwordx4 v77, s[42:43]
	ds_read_b128 v[36:39], v84 offset:20480
	v_mfma_f32_32x32x16_f16 a[32:47], v[40:43], v[56:59], a[32:47]
	ds_read_b128 v[40:43], v84 offset:21504
	v_mfma_f32_32x32x16_f16 a[16:31], v[44:47], v[56:59], a[16:31]
	s_add_u32 m0, s48, 0x0
	s_add_u32 s44, s44, 0x1800
	s_addc_u32 s45, s45, 0
	global_load_lds_dwordx4 v78, s[44:45]
	ds_read_b128 v[44:47], v84 offset:22528
	v_mfma_f32_32x32x16_f16 a[0:15], v[48:51], v[56:59], a[0:15]
	ds_read_b128 v[48:51], v84 offset:23552
	s_waitcnt lgkmcnt(6)
	s_nop 0
	v_mfma_f32_32x32x16_f16 a[80:95], v[4:7], v[60:63], a[80:95]
	s_waitcnt vmcnt(23)
	ds_write_b128 v81, v[116:119]
	ds_write_b128 v81, v[120:123] offset:1024
	s_nop 0
	v_mfma_f32_32x32x16_f16 a[64:79], v[8:11], v[60:63], a[64:79]
	ds_write_b128 v81, v[124:127] offset:2048
	ds_write_b128 v81, v[128:131] offset:3072
	v_mfma_f32_32x32x16_f16 a[48:63], v[12:15], v[60:63], a[48:63]
	ds_read_b128 v[100:103], v95
	ds_read_b128 v[104:107], v96
	ds_read_b128 v[108:111], v97
	ds_read_b128 v[112:115], v94
	s_waitcnt vmcnt(10)
	s_waitcnt lgkmcnt(8)
	s_barrier
	ds_read_b128 v[4:7], v84 offset:54208
	ds_read_b128 v[8:11], v84 offset:55232
	ds_read_b128 v[12:15], v84 offset:56256
	s_nop 0
	v_mfma_f32_32x32x16_f16 a[32:47], v[16:19], v[60:63], a[32:47]
	ds_read_b128 v[16:19], v84 offset:57280
	v_mfma_f32_32x32x16_f16 a[16:31], v[20:23], v[60:63], a[16:31]
	ds_read_b128 v[20:23], v84 offset:58304
	v_mfma_f32_32x32x16_f16 a[0:15], v[24:27], v[60:63], a[0:15]
	ds_read_b128 v[24:27], v84 offset:59328
	s_waitcnt lgkmcnt(6)
	s_nop 0
	v_mfma_f32_32x32x16_f16 a[80:95], v[28:31], v[0:3], a[80:95]
	s_add_u32 m0, s46, 0x3000
	s_add_u32 s40, s40, 0x1800
	s_addc_u32 s41, s41, 0
	global_load_lds_dwordx4 v76, s[40:41]
	ds_read_b128 v[28:31], v84 offset:60352
	s_nop 0
	v_mfma_f32_32x32x16_f16 a[64:79], v[32:35], v[0:3], a[64:79]
	global_load_dwordx4 v[116:119], v64, s[4:5] offset:768
	global_load_dwordx4 v[120:123], v66, s[4:5] offset:768
	ds_read_b128 v[32:35], v84 offset:61376
	v_mfma_f32_32x32x16_f16 a[48:63], v[36:39], v[0:3], a[48:63]
	s_add_u32 m0, s47, 0x3000
	s_add_u32 s42, s42, 0x1800
	s_addc_u32 s43, s43, 0
	global_load_lds_dwordx4 v77, s[42:43]
	ds_read_b128 v[36:39], v84 offset:62400
	s_nop 0
	v_mfma_f32_32x32x16_f16 a[32:47], v[40:43], v[0:3], a[32:47]
	global_load_dwordx4 v[124:127], v68, s[4:5] offset:768
	global_load_dwordx4 v[128:131], v70, s[4:5] offset:768
	ds_read_b128 v[40:43], v84 offset:63424
	v_mfma_f32_32x32x16_f16 a[16:31], v[44:47], v[0:3], a[16:31]
	s_add_u32 m0, s48, 0x3000
	s_add_u32 s44, s44, 0x1800
	s_addc_u32 s45, s45, 0
	global_load_lds_dwordx4 v78, s[44:45]
	ds_read_b128 v[44:47], v84 offset:64448
	s_nop 0
	v_mfma_f32_32x32x16_f16 a[0:15], v[48:51], v[0:3], a[0:15]
	ds_read_b128 v[48:51], v84 offset:65472
	s_waitcnt lgkmcnt(6)
	s_nop 0
	v_mfma_f32_32x32x16_f16 a[80:95], v[4:7], v[100:103], a[80:95]
	v_mfma_f32_32x32x16_f16 a[64:79], v[8:11], v[100:103], a[64:79]
	v_mfma_f32_32x32x16_f16 a[48:63], v[12:15], v[100:103], a[48:63]
	s_waitcnt vmcnt(10)
	s_waitcnt lgkmcnt(0)
	s_barrier
	ds_read_b128 v[4:7], v98
	ds_read_b128 v[8:11], v98 offset:1024
	ds_read_b128 v[12:15], v98 offset:2048
	s_nop 0
	v_mfma_f32_32x32x16_f16 a[32:47], v[16:19], v[100:103], a[32:47]
	ds_read_b128 v[16:19], v98 offset:3072
	v_mfma_f32_32x32x16_f16 a[16:31], v[20:23], v[100:103], a[16:31]
	ds_read_b128 v[20:23], v98 offset:4096
	v_mfma_f32_32x32x16_f16 a[0:15], v[24:27], v[100:103], a[0:15]
	ds_read_b128 v[24:27], v98 offset:5120
	v_mfma_f32_32x32x16_f16 a[80:95], v[28:31], v[104:107], a[80:95]
	s_add_u32 m0, s46, 0xd3c0
	s_add_u32 s40, s40, 0x1800
	s_addc_u32 s41, s41, 0
	global_load_lds_dwordx4 v76, s[40:41]
	ds_read_b128 v[28:31], v98 offset:6144
	s_nop 0
	v_mfma_f32_32x32x16_f16 a[64:79], v[32:35], v[104:107], a[64:79]
	ds_read_b128 v[32:35], v98 offset:7168
	v_mfma_f32_32x32x16_f16 a[48:63], v[36:39], v[104:107], a[48:63]
	s_add_u32 m0, s47, 0xd3c0
	s_add_u32 s42, s42, 0x1800
	s_addc_u32 s43, s43, 0
	global_load_lds_dwordx4 v77, s[42:43]
	ds_read_b128 v[36:39], v98 offset:8192
	s_nop 0
	v_mfma_f32_32x32x16_f16 a[32:47], v[40:43], v[104:107], a[32:47]
	ds_read_b128 v[40:43], v98 offset:9216
	v_mfma_f32_32x32x16_f16 a[16:31], v[44:47], v[104:107], a[16:31]
	s_add_u32 m0, s48, 0xd3c0
	s_add_u32 s44, s44, 0x1800
	s_addc_u32 s45, s45, 0
	global_load_lds_dwordx4 v78, s[44:45]
	ds_read_b128 v[44:47], v98 offset:10240
	s_nop 0
	v_mfma_f32_32x32x16_f16 a[0:15], v[48:51], v[104:107], a[0:15]
	ds_read_b128 v[48:51], v98 offset:11264
	s_waitcnt lgkmcnt(6)
	s_nop 0
	v_mfma_f32_32x32x16_f16 a[80:95], v[4:7], v[108:111], a[80:95]
	s_waitcnt vmcnt(24)
	ds_write_b128 v81, v[132:135]
	ds_write_b128 v81, v[136:139] offset:1024
	s_nop 0
	v_mfma_f32_32x32x16_f16 a[64:79], v[8:11], v[108:111], a[64:79]
	ds_write_b128 v81, v[140:143] offset:2048
	ds_write_b128 v81, v[144:147] offset:3072
	v_mfma_f32_32x32x16_f16 a[48:63], v[12:15], v[108:111], a[48:63]
	ds_read_b128 v[52:55], v95
	ds_read_b128 v[56:59], v96
	ds_read_b128 v[60:63], v97
	ds_read_b128 v[0:3], v94
	s_waitcnt vmcnt(10)
	s_waitcnt lgkmcnt(8)
	s_barrier
	ds_read_b128 v[4:7], v84 offset:0
	ds_read_b128 v[8:11], v84 offset:1024
	ds_read_b128 v[12:15], v84 offset:2048
	s_nop 0
	v_mfma_f32_32x32x16_f16 a[32:47], v[16:19], v[108:111], a[32:47]
	ds_read_b128 v[16:19], v84 offset:3072
	v_mfma_f32_32x32x16_f16 a[16:31], v[20:23], v[108:111], a[16:31]
	ds_read_b128 v[20:23], v84 offset:4096
	v_mfma_f32_32x32x16_f16 a[0:15], v[24:27], v[108:111], a[0:15]
	ds_read_b128 v[24:27], v84 offset:5120
	s_waitcnt lgkmcnt(6)
	s_nop 0
	v_mfma_f32_32x32x16_f16 a[80:95], v[28:31], v[112:115], a[80:95]
	s_add_u32 m0, s46, 0x103c0
	s_add_u32 s40, s40, 0x1800
	s_addc_u32 s41, s41, 0
	global_load_lds_dwordx4 v76, s[40:41]
	ds_read_b128 v[28:31], v84 offset:6144
	s_nop 0
	v_mfma_f32_32x32x16_f16 a[64:79], v[32:35], v[112:115], a[64:79]
	global_load_dwordx4 v[132:135], v64, s[4:5] offset:896
	global_load_dwordx4 v[136:139], v66, s[4:5] offset:896
	ds_read_b128 v[32:35], v84 offset:7168
	v_mfma_f32_32x32x16_f16 a[48:63], v[36:39], v[112:115], a[48:63]
	s_add_u32 m0, s47, 0x103c0
	s_add_u32 s42, s42, 0x1800
	s_addc_u32 s43, s43, 0
	global_load_lds_dwordx4 v77, s[42:43]
	ds_read_b128 v[36:39], v84 offset:8192
	s_nop 0
	v_mfma_f32_32x32x16_f16 a[32:47], v[40:43], v[112:115], a[32:47]
	global_load_dwordx4 v[140:143], v68, s[4:5] offset:896
	global_load_dwordx4 v[144:147], v70, s[4:5] offset:896
	ds_read_b128 v[40:43], v84 offset:9216
	v_mfma_f32_32x32x16_f16 a[16:31], v[44:47], v[112:115], a[16:31]
	s_add_u32 m0, s48, 0x103c0
	s_add_u32 s44, s44, 0x1800
	s_addc_u32 s45, s45, 0
	global_load_lds_dwordx4 v78, s[44:45]
	ds_read_b128 v[44:47], v84 offset:10240
	s_nop 0
	v_mfma_f32_32x32x16_f16 a[0:15], v[48:51], v[112:115], a[0:15]
	ds_read_b128 v[48:51], v84 offset:11264
	s_waitcnt lgkmcnt(6)
	s_nop 0
	v_mfma_f32_32x32x16_f16 a[80:95], v[4:7], v[52:55], a[80:95]
	v_mfma_f32_32x32x16_f16 a[64:79], v[8:11], v[52:55], a[64:79]
	v_mfma_f32_32x32x16_f16 a[48:63], v[12:15], v[52:55], a[48:63]
	s_waitcnt vmcnt(10)
	s_waitcnt lgkmcnt(0)
	s_barrier
	ds_read_b128 v[4:7], v84 offset:12288
	ds_read_b128 v[8:11], v84 offset:13312
	ds_read_b128 v[12:15], v84 offset:14336
	s_nop 0
	v_mfma_f32_32x32x16_f16 a[32:47], v[16:19], v[52:55], a[32:47]
	ds_read_b128 v[16:19], v84 offset:15360
	v_mfma_f32_32x32x16_f16 a[16:31], v[20:23], v[52:55], a[16:31]
	ds_read_b128 v[20:23], v84 offset:16384
	v_mfma_f32_32x32x16_f16 a[0:15], v[24:27], v[52:55], a[0:15]
	ds_read_b128 v[24:27], v84 offset:17408
	v_mfma_f32_32x32x16_f16 a[80:95], v[28:31], v[56:59], a[80:95]
	s_add_u32 m0, s46, 0x0
	s_add_u32 s40, s40, 0x1800
	s_addc_u32 s41, s41, 0
	global_load_lds_dwordx4 v76, s[40:41]
	ds_read_b128 v[28:31], v84 offset:18432
	v_mfma_f32_32x32x16_f16 a[64:79], v[32:35], v[56:59], a[64:79]
	ds_read_b128 v[32:35], v84 offset:19456
	v_mfma_f32_32x32x16_f16 a[48:63], v[36:39], v[56:59], a[48:63]
	s_add_u32 m0, s47, 0x0
	s_add_u32 s42, s42, 0x1800
	s_addc_u32 s43, s43, 0
	global_load_lds_dwordx4 v77, s[42:43]
	ds_read_b128 v[36:39], v84 offset:20480
	v_mfma_f32_32x32x16_f16 a[32:47], v[40:43], v[56:59], a[32:47]
	ds_read_b128 v[40:43], v84 offset:21504
	v_mfma_f32_32x32x16_f16 a[16:31], v[44:47], v[56:59], a[16:31]
	s_add_u32 m0, s48, 0x0
	s_add_u32 s44, s44, 0x1800
	s_addc_u32 s45, s45, 0
	global_load_lds_dwordx4 v78, s[44:45]
	ds_read_b128 v[44:47], v84 offset:22528
	v_mfma_f32_32x32x16_f16 a[0:15], v[48:51], v[56:59], a[0:15]
	ds_read_b128 v[48:51], v84 offset:23552
	s_waitcnt lgkmcnt(6)
	s_nop 0
	v_mfma_f32_32x32x16_f16 a[80:95], v[4:7], v[60:63], a[80:95]
	s_waitcnt vmcnt(24)
	ds_write_b128 v81, v[148:151]
	ds_write_b128 v81, v[152:155] offset:1024
	s_nop 0
	v_mfma_f32_32x32x16_f16 a[64:79], v[8:11], v[60:63], a[64:79]
	ds_write_b128 v81, v[156:159] offset:2048
	ds_write_b128 v81, v[72:75] offset:3072
	v_mfma_f32_32x32x16_f16 a[48:63], v[12:15], v[60:63], a[48:63]
	ds_read_b128 v[100:103], v95
	ds_read_b128 v[104:107], v96
	ds_read_b128 v[108:111], v97
	ds_read_b128 v[112:115], v94
	s_waitcnt vmcnt(10)
	s_waitcnt lgkmcnt(8)
	s_barrier
	ds_read_b128 v[4:7], v84 offset:54208
	ds_read_b128 v[8:11], v84 offset:55232
	ds_read_b128 v[12:15], v84 offset:56256
	s_nop 0
	v_mfma_f32_32x32x16_f16 a[32:47], v[16:19], v[60:63], a[32:47]
	ds_read_b128 v[16:19], v84 offset:57280
	v_mfma_f32_32x32x16_f16 a[16:31], v[20:23], v[60:63], a[16:31]
	ds_read_b128 v[20:23], v84 offset:58304
	v_mfma_f32_32x32x16_f16 a[0:15], v[24:27], v[60:63], a[0:15]
	ds_read_b128 v[24:27], v84 offset:59328
	s_waitcnt lgkmcnt(6)
	s_nop 0
	v_mfma_f32_32x32x16_f16 a[80:95], v[28:31], v[0:3], a[80:95]
	s_add_u32 m0, s46, 0x3000
	s_add_u32 s40, s40, 0x1800
	s_addc_u32 s41, s41, 0
	global_load_lds_dwordx4 v76, s[40:41]
	ds_read_b128 v[28:31], v84 offset:60352
	s_nop 0
	v_mfma_f32_32x32x16_f16 a[64:79], v[32:35], v[0:3], a[64:79]
	global_load_dwordx4 v[148:151], v64, s[4:5] offset:1024
	global_load_dwordx4 v[152:155], v66, s[4:5] offset:1024
	ds_read_b128 v[32:35], v84 offset:61376
	v_mfma_f32_32x32x16_f16 a[48:63], v[36:39], v[0:3], a[48:63]
	s_add_u32 m0, s47, 0x3000
	s_add_u32 s42, s42, 0x1800
	s_addc_u32 s43, s43, 0
	global_load_lds_dwordx4 v77, s[42:43]
	ds_read_b128 v[36:39], v84 offset:62400
	s_nop 0
	v_mfma_f32_32x32x16_f16 a[32:47], v[40:43], v[0:3], a[32:47]
	global_load_dwordx4 v[156:159], v68, s[4:5] offset:1024
	global_load_dwordx4 v[72:75], v70, s[4:5] offset:1024
	ds_read_b128 v[40:43], v84 offset:63424
	v_mfma_f32_32x32x16_f16 a[16:31], v[44:47], v[0:3], a[16:31]
	s_add_u32 m0, s48, 0x3000
	s_add_u32 s44, s44, 0x1800
	s_addc_u32 s45, s45, 0
	global_load_lds_dwordx4 v78, s[44:45]
	ds_read_b128 v[44:47], v84 offset:64448
	s_nop 0
	v_mfma_f32_32x32x16_f16 a[0:15], v[48:51], v[0:3], a[0:15]
	ds_read_b128 v[48:51], v84 offset:65472
	s_waitcnt lgkmcnt(6)
	s_nop 0
	v_mfma_f32_32x32x16_f16 a[80:95], v[4:7], v[100:103], a[80:95]
	v_mfma_f32_32x32x16_f16 a[64:79], v[8:11], v[100:103], a[64:79]
	v_mfma_f32_32x32x16_f16 a[48:63], v[12:15], v[100:103], a[48:63]
	s_waitcnt vmcnt(10)
	s_waitcnt lgkmcnt(0)
	s_barrier
	ds_read_b128 v[4:7], v98
	ds_read_b128 v[8:11], v98 offset:1024
	ds_read_b128 v[12:15], v98 offset:2048
	s_nop 0
	v_mfma_f32_32x32x16_f16 a[32:47], v[16:19], v[100:103], a[32:47]
	ds_read_b128 v[16:19], v98 offset:3072
	v_mfma_f32_32x32x16_f16 a[16:31], v[20:23], v[100:103], a[16:31]
	ds_read_b128 v[20:23], v98 offset:4096
	v_mfma_f32_32x32x16_f16 a[0:15], v[24:27], v[100:103], a[0:15]
	ds_read_b128 v[24:27], v98 offset:5120
	v_mfma_f32_32x32x16_f16 a[80:95], v[28:31], v[104:107], a[80:95]
	s_add_u32 m0, s46, 0xd3c0
	s_add_u32 s40, s40, 0x1800
	s_addc_u32 s41, s41, 0
	global_load_lds_dwordx4 v76, s[40:41]
	ds_read_b128 v[28:31], v98 offset:6144
	s_nop 0
	v_mfma_f32_32x32x16_f16 a[64:79], v[32:35], v[104:107], a[64:79]
	ds_read_b128 v[32:35], v98 offset:7168
	v_mfma_f32_32x32x16_f16 a[48:63], v[36:39], v[104:107], a[48:63]
	s_add_u32 m0, s47, 0xd3c0
	s_add_u32 s42, s42, 0x1800
	s_addc_u32 s43, s43, 0
	global_load_lds_dwordx4 v77, s[42:43]
	ds_read_b128 v[36:39], v98 offset:8192
	s_nop 0
	v_mfma_f32_32x32x16_f16 a[32:47], v[40:43], v[104:107], a[32:47]
	ds_read_b128 v[40:43], v98 offset:9216
	v_mfma_f32_32x32x16_f16 a[16:31], v[44:47], v[104:107], a[16:31]
	s_add_u32 m0, s48, 0xd3c0
	s_add_u32 s44, s44, 0x1800
	s_addc_u32 s45, s45, 0
	global_load_lds_dwordx4 v78, s[44:45]
	ds_read_b128 v[44:47], v98 offset:10240
	s_nop 0
	v_mfma_f32_32x32x16_f16 a[0:15], v[48:51], v[104:107], a[0:15]
	ds_read_b128 v[48:51], v98 offset:11264
	s_waitcnt lgkmcnt(6)
	s_nop 0
	v_mfma_f32_32x32x16_f16 a[80:95], v[4:7], v[108:111], a[80:95]
	s_waitcnt vmcnt(24)
	ds_write_b128 v81, v[116:119]
	ds_write_b128 v81, v[120:123] offset:1024
	s_nop 0
	v_mfma_f32_32x32x16_f16 a[64:79], v[8:11], v[108:111], a[64:79]
	ds_write_b128 v81, v[124:127] offset:2048
	ds_write_b128 v81, v[128:131] offset:3072
	v_mfma_f32_32x32x16_f16 a[48:63], v[12:15], v[108:111], a[48:63]
	ds_read_b128 v[52:55], v95
	ds_read_b128 v[56:59], v96
	ds_read_b128 v[60:63], v97
	ds_read_b128 v[0:3], v94
	s_waitcnt vmcnt(10)
	s_waitcnt lgkmcnt(8)
	s_barrier
	ds_read_b128 v[4:7], v84 offset:0
	ds_read_b128 v[8:11], v84 offset:1024
	ds_read_b128 v[12:15], v84 offset:2048
	s_nop 0
	v_mfma_f32_32x32x16_f16 a[32:47], v[16:19], v[108:111], a[32:47]
	ds_read_b128 v[16:19], v84 offset:3072
	v_mfma_f32_32x32x16_f16 a[16:31], v[20:23], v[108:111], a[16:31]
	ds_read_b128 v[20:23], v84 offset:4096
	v_mfma_f32_32x32x16_f16 a[0:15], v[24:27], v[108:111], a[0:15]
	ds_read_b128 v[24:27], v84 offset:5120
	s_waitcnt lgkmcnt(6)
	s_nop 0
	v_mfma_f32_32x32x16_f16 a[80:95], v[28:31], v[112:115], a[80:95]
	s_add_u32 m0, s46, 0x103c0
	s_add_u32 s40, s40, 0x1800
	s_addc_u32 s41, s41, 0
	global_load_lds_dwordx4 v76, s[40:41]
	ds_read_b128 v[28:31], v84 offset:6144
	s_nop 0
	v_mfma_f32_32x32x16_f16 a[64:79], v[32:35], v[112:115], a[64:79]
	global_load_dwordx4 v[116:119], v64, s[4:5] offset:1152
	global_load_dwordx4 v[120:123], v66, s[4:5] offset:1152
	ds_read_b128 v[32:35], v84 offset:7168
	v_mfma_f32_32x32x16_f16 a[48:63], v[36:39], v[112:115], a[48:63]
	s_add_u32 m0, s47, 0x103c0
	s_add_u32 s42, s42, 0x1800
	s_addc_u32 s43, s43, 0
	global_load_lds_dwordx4 v77, s[42:43]
	ds_read_b128 v[36:39], v84 offset:8192
	s_nop 0
	v_mfma_f32_32x32x16_f16 a[32:47], v[40:43], v[112:115], a[32:47]
	global_load_dwordx4 v[124:127], v68, s[4:5] offset:1152
	global_load_dwordx4 v[128:131], v70, s[4:5] offset:1152
	ds_read_b128 v[40:43], v84 offset:9216
	v_mfma_f32_32x32x16_f16 a[16:31], v[44:47], v[112:115], a[16:31]
	s_add_u32 m0, s48, 0x103c0
	s_add_u32 s44, s44, 0x1800
	s_addc_u32 s45, s45, 0
	global_load_lds_dwordx4 v78, s[44:45]
	ds_read_b128 v[44:47], v84 offset:10240
	s_nop 0
	v_mfma_f32_32x32x16_f16 a[0:15], v[48:51], v[112:115], a[0:15]
	ds_read_b128 v[48:51], v84 offset:11264
	s_waitcnt lgkmcnt(6)
	s_nop 0
	v_mfma_f32_32x32x16_f16 a[80:95], v[4:7], v[52:55], a[80:95]
	v_mfma_f32_32x32x16_f16 a[64:79], v[8:11], v[52:55], a[64:79]
	v_mfma_f32_32x32x16_f16 a[48:63], v[12:15], v[52:55], a[48:63]
	s_waitcnt vmcnt(10)
	s_waitcnt lgkmcnt(0)
	s_barrier
	ds_read_b128 v[4:7], v84 offset:12288
	ds_read_b128 v[8:11], v84 offset:13312
	ds_read_b128 v[12:15], v84 offset:14336
	s_nop 0
	v_mfma_f32_32x32x16_f16 a[32:47], v[16:19], v[52:55], a[32:47]
	ds_read_b128 v[16:19], v84 offset:15360
	v_mfma_f32_32x32x16_f16 a[16:31], v[20:23], v[52:55], a[16:31]
	ds_read_b128 v[20:23], v84 offset:16384
	v_mfma_f32_32x32x16_f16 a[0:15], v[24:27], v[52:55], a[0:15]
	ds_read_b128 v[24:27], v84 offset:17408
	v_mfma_f32_32x32x16_f16 a[80:95], v[28:31], v[56:59], a[80:95]
	s_add_u32 m0, s46, 0x0
	s_add_u32 s40, s40, 0x1800
	s_addc_u32 s41, s41, 0
	global_load_lds_dwordx4 v76, s[40:41]
	ds_read_b128 v[28:31], v84 offset:18432
	v_mfma_f32_32x32x16_f16 a[64:79], v[32:35], v[56:59], a[64:79]
	ds_read_b128 v[32:35], v84 offset:19456
	v_mfma_f32_32x32x16_f16 a[48:63], v[36:39], v[56:59], a[48:63]
	s_add_u32 m0, s47, 0x0
	s_add_u32 s42, s42, 0x1800
	s_addc_u32 s43, s43, 0
	global_load_lds_dwordx4 v77, s[42:43]
	ds_read_b128 v[36:39], v84 offset:20480
	v_mfma_f32_32x32x16_f16 a[32:47], v[40:43], v[56:59], a[32:47]
	ds_read_b128 v[40:43], v84 offset:21504
	v_mfma_f32_32x32x16_f16 a[16:31], v[44:47], v[56:59], a[16:31]
	s_add_u32 m0, s48, 0x0
	s_add_u32 s44, s44, 0x1800
	s_addc_u32 s45, s45, 0
	global_load_lds_dwordx4 v78, s[44:45]
	ds_read_b128 v[44:47], v84 offset:22528
	v_mfma_f32_32x32x16_f16 a[0:15], v[48:51], v[56:59], a[0:15]
	ds_read_b128 v[48:51], v84 offset:23552
	s_waitcnt lgkmcnt(6)
	s_nop 0
	v_mfma_f32_32x32x16_f16 a[80:95], v[4:7], v[60:63], a[80:95]
	s_waitcnt vmcnt(24)
	ds_write_b128 v81, v[132:135]
	ds_write_b128 v81, v[136:139] offset:1024
	s_nop 0
	v_mfma_f32_32x32x16_f16 a[64:79], v[8:11], v[60:63], a[64:79]
	ds_write_b128 v81, v[140:143] offset:2048
	ds_write_b128 v81, v[144:147] offset:3072
	v_mfma_f32_32x32x16_f16 a[48:63], v[12:15], v[60:63], a[48:63]
	ds_read_b128 v[100:103], v95
	ds_read_b128 v[104:107], v96
	ds_read_b128 v[108:111], v97
	ds_read_b128 v[112:115], v94
	s_waitcnt vmcnt(10)
	s_waitcnt lgkmcnt(8)
	s_barrier
	ds_read_b128 v[4:7], v84 offset:54208
	ds_read_b128 v[8:11], v84 offset:55232
	ds_read_b128 v[12:15], v84 offset:56256
	s_nop 0
	v_mfma_f32_32x32x16_f16 a[32:47], v[16:19], v[60:63], a[32:47]
	ds_read_b128 v[16:19], v84 offset:57280
	v_mfma_f32_32x32x16_f16 a[16:31], v[20:23], v[60:63], a[16:31]
	ds_read_b128 v[20:23], v84 offset:58304
	v_mfma_f32_32x32x16_f16 a[0:15], v[24:27], v[60:63], a[0:15]
	ds_read_b128 v[24:27], v84 offset:59328
	s_waitcnt lgkmcnt(6)
	s_nop 0
	v_mfma_f32_32x32x16_f16 a[80:95], v[28:31], v[0:3], a[80:95]
	s_add_u32 m0, s46, 0x3000
	s_add_u32 s40, s40, 0x1800
	s_addc_u32 s41, s41, 0
	global_load_lds_dwordx4 v76, s[40:41]
	ds_read_b128 v[28:31], v84 offset:60352
	s_nop 0
	v_mfma_f32_32x32x16_f16 a[64:79], v[32:35], v[0:3], a[64:79]
	global_load_dwordx4 v[132:135], v64, s[4:5] offset:1280
	global_load_dwordx4 v[136:139], v66, s[4:5] offset:1280
	ds_read_b128 v[32:35], v84 offset:61376
	v_mfma_f32_32x32x16_f16 a[48:63], v[36:39], v[0:3], a[48:63]
	s_add_u32 m0, s47, 0x3000
	s_add_u32 s42, s42, 0x1800
	s_addc_u32 s43, s43, 0
	global_load_lds_dwordx4 v77, s[42:43]
	ds_read_b128 v[36:39], v84 offset:62400
	s_nop 0
	v_mfma_f32_32x32x16_f16 a[32:47], v[40:43], v[0:3], a[32:47]
	global_load_dwordx4 v[140:143], v68, s[4:5] offset:1280
	global_load_dwordx4 v[144:147], v70, s[4:5] offset:1280
	ds_read_b128 v[40:43], v84 offset:63424
	v_mfma_f32_32x32x16_f16 a[16:31], v[44:47], v[0:3], a[16:31]
	s_add_u32 m0, s48, 0x3000
	s_add_u32 s44, s44, 0x1800
	s_addc_u32 s45, s45, 0
	global_load_lds_dwordx4 v78, s[44:45]
	ds_read_b128 v[44:47], v84 offset:64448
	s_nop 0
	v_mfma_f32_32x32x16_f16 a[0:15], v[48:51], v[0:3], a[0:15]
	ds_read_b128 v[48:51], v84 offset:65472
	s_waitcnt lgkmcnt(6)
	s_nop 0
	v_mfma_f32_32x32x16_f16 a[80:95], v[4:7], v[100:103], a[80:95]
	v_mfma_f32_32x32x16_f16 a[64:79], v[8:11], v[100:103], a[64:79]
	v_mfma_f32_32x32x16_f16 a[48:63], v[12:15], v[100:103], a[48:63]
	s_waitcnt vmcnt(10)
	s_waitcnt lgkmcnt(0)
	s_barrier
	ds_read_b128 v[4:7], v98
	ds_read_b128 v[8:11], v98 offset:1024
	ds_read_b128 v[12:15], v98 offset:2048
	s_nop 0
	v_mfma_f32_32x32x16_f16 a[32:47], v[16:19], v[100:103], a[32:47]
	ds_read_b128 v[16:19], v98 offset:3072
	v_mfma_f32_32x32x16_f16 a[16:31], v[20:23], v[100:103], a[16:31]
	ds_read_b128 v[20:23], v98 offset:4096
	v_mfma_f32_32x32x16_f16 a[0:15], v[24:27], v[100:103], a[0:15]
	ds_read_b128 v[24:27], v98 offset:5120
	v_mfma_f32_32x32x16_f16 a[80:95], v[28:31], v[104:107], a[80:95]
	s_add_u32 m0, s46, 0xd3c0
	s_add_u32 s40, s40, 0x1800
	s_addc_u32 s41, s41, 0
	global_load_lds_dwordx4 v76, s[40:41]
	ds_read_b128 v[28:31], v98 offset:6144
	s_nop 0
	v_mfma_f32_32x32x16_f16 a[64:79], v[32:35], v[104:107], a[64:79]
	ds_read_b128 v[32:35], v98 offset:7168
	v_mfma_f32_32x32x16_f16 a[48:63], v[36:39], v[104:107], a[48:63]
	s_add_u32 m0, s47, 0xd3c0
	s_add_u32 s42, s42, 0x1800
	s_addc_u32 s43, s43, 0
	global_load_lds_dwordx4 v77, s[42:43]
	ds_read_b128 v[36:39], v98 offset:8192
	s_nop 0
	v_mfma_f32_32x32x16_f16 a[32:47], v[40:43], v[104:107], a[32:47]
	ds_read_b128 v[40:43], v98 offset:9216
	v_mfma_f32_32x32x16_f16 a[16:31], v[44:47], v[104:107], a[16:31]
	s_add_u32 m0, s48, 0xd3c0
	s_add_u32 s44, s44, 0x1800
	s_addc_u32 s45, s45, 0
	global_load_lds_dwordx4 v78, s[44:45]
	ds_read_b128 v[44:47], v98 offset:10240
	s_nop 0
	v_mfma_f32_32x32x16_f16 a[0:15], v[48:51], v[104:107], a[0:15]
	ds_read_b128 v[48:51], v98 offset:11264
	s_waitcnt lgkmcnt(6)
	s_nop 0
	v_mfma_f32_32x32x16_f16 a[80:95], v[4:7], v[108:111], a[80:95]
	s_waitcnt vmcnt(24)
	ds_write_b128 v81, v[148:151]
	ds_write_b128 v81, v[152:155] offset:1024
	s_nop 0
	v_mfma_f32_32x32x16_f16 a[64:79], v[8:11], v[108:111], a[64:79]
	ds_write_b128 v81, v[156:159] offset:2048
	ds_write_b128 v81, v[72:75] offset:3072
	v_mfma_f32_32x32x16_f16 a[48:63], v[12:15], v[108:111], a[48:63]
	ds_read_b128 v[52:55], v95
	ds_read_b128 v[56:59], v96
	ds_read_b128 v[60:63], v97
	ds_read_b128 v[0:3], v94
	s_waitcnt vmcnt(10)
	s_waitcnt lgkmcnt(8)
	s_barrier
	ds_read_b128 v[4:7], v84 offset:0
	ds_read_b128 v[8:11], v84 offset:1024
	ds_read_b128 v[12:15], v84 offset:2048
	s_nop 0
	v_mfma_f32_32x32x16_f16 a[32:47], v[16:19], v[108:111], a[32:47]
	ds_read_b128 v[16:19], v84 offset:3072
	v_mfma_f32_32x32x16_f16 a[16:31], v[20:23], v[108:111], a[16:31]
	ds_read_b128 v[20:23], v84 offset:4096
	v_mfma_f32_32x32x16_f16 a[0:15], v[24:27], v[108:111], a[0:15]
	ds_read_b128 v[24:27], v84 offset:5120
	s_waitcnt lgkmcnt(6)
	s_nop 0
	v_mfma_f32_32x32x16_f16 a[80:95], v[28:31], v[112:115], a[80:95]
	s_add_u32 m0, s46, 0x103c0
	s_add_u32 s40, s40, 0x1800
	s_addc_u32 s41, s41, 0
	global_load_lds_dwordx4 v76, s[40:41]
	ds_read_b128 v[28:31], v84 offset:6144
	s_nop 0
	v_mfma_f32_32x32x16_f16 a[64:79], v[32:35], v[112:115], a[64:79]
	global_load_dwordx4 v[148:151], v64, s[4:5] offset:1408
	global_load_dwordx4 v[152:155], v66, s[4:5] offset:1408
	ds_read_b128 v[32:35], v84 offset:7168
	v_mfma_f32_32x32x16_f16 a[48:63], v[36:39], v[112:115], a[48:63]
	s_add_u32 m0, s47, 0x103c0
	s_add_u32 s42, s42, 0x1800
	s_addc_u32 s43, s43, 0
	global_load_lds_dwordx4 v77, s[42:43]
	ds_read_b128 v[36:39], v84 offset:8192
	s_nop 0
	v_mfma_f32_32x32x16_f16 a[32:47], v[40:43], v[112:115], a[32:47]
	global_load_dwordx4 v[156:159], v68, s[4:5] offset:1408
	global_load_dwordx4 v[72:75], v70, s[4:5] offset:1408
	ds_read_b128 v[40:43], v84 offset:9216
	v_mfma_f32_32x32x16_f16 a[16:31], v[44:47], v[112:115], a[16:31]
	s_add_u32 m0, s48, 0x103c0
	s_add_u32 s44, s44, 0x1800
	s_addc_u32 s45, s45, 0
	global_load_lds_dwordx4 v78, s[44:45]
	ds_read_b128 v[44:47], v84 offset:10240
	s_nop 0
	v_mfma_f32_32x32x16_f16 a[0:15], v[48:51], v[112:115], a[0:15]
	ds_read_b128 v[48:51], v84 offset:11264
	s_waitcnt lgkmcnt(6)
	s_nop 0
	v_mfma_f32_32x32x16_f16 a[80:95], v[4:7], v[52:55], a[80:95]
	v_mfma_f32_32x32x16_f16 a[64:79], v[8:11], v[52:55], a[64:79]
	v_mfma_f32_32x32x16_f16 a[48:63], v[12:15], v[52:55], a[48:63]
	s_waitcnt vmcnt(10)
	s_waitcnt lgkmcnt(0)
	s_barrier
	ds_read_b128 v[4:7], v84 offset:12288
	ds_read_b128 v[8:11], v84 offset:13312
	ds_read_b128 v[12:15], v84 offset:14336
	s_nop 0
	v_mfma_f32_32x32x16_f16 a[32:47], v[16:19], v[52:55], a[32:47]
	ds_read_b128 v[16:19], v84 offset:15360
	v_mfma_f32_32x32x16_f16 a[16:31], v[20:23], v[52:55], a[16:31]
	ds_read_b128 v[20:23], v84 offset:16384
	v_mfma_f32_32x32x16_f16 a[0:15], v[24:27], v[52:55], a[0:15]
	ds_read_b128 v[24:27], v84 offset:17408
	v_mfma_f32_32x32x16_f16 a[80:95], v[28:31], v[56:59], a[80:95]
	s_add_u32 m0, s46, 0x0
	s_add_u32 s40, s40, 0x1800
	s_addc_u32 s41, s41, 0
	global_load_lds_dwordx4 v76, s[40:41]
	ds_read_b128 v[28:31], v84 offset:18432
	v_mfma_f32_32x32x16_f16 a[64:79], v[32:35], v[56:59], a[64:79]
	ds_read_b128 v[32:35], v84 offset:19456
	v_mfma_f32_32x32x16_f16 a[48:63], v[36:39], v[56:59], a[48:63]
	s_add_u32 m0, s47, 0x0
	s_add_u32 s42, s42, 0x1800
	s_addc_u32 s43, s43, 0
	global_load_lds_dwordx4 v77, s[42:43]
	ds_read_b128 v[36:39], v84 offset:20480
	v_mfma_f32_32x32x16_f16 a[32:47], v[40:43], v[56:59], a[32:47]
	ds_read_b128 v[40:43], v84 offset:21504
	v_mfma_f32_32x32x16_f16 a[16:31], v[44:47], v[56:59], a[16:31]
	s_add_u32 m0, s48, 0x0
	s_add_u32 s44, s44, 0x1800
	s_addc_u32 s45, s45, 0
	global_load_lds_dwordx4 v78, s[44:45]
	ds_read_b128 v[44:47], v84 offset:22528
	v_mfma_f32_32x32x16_f16 a[0:15], v[48:51], v[56:59], a[0:15]
	ds_read_b128 v[48:51], v84 offset:23552
	s_waitcnt lgkmcnt(6)
	s_nop 0
	v_mfma_f32_32x32x16_f16 a[80:95], v[4:7], v[60:63], a[80:95]
	s_waitcnt vmcnt(24)
	ds_write_b128 v81, v[116:119]
	ds_write_b128 v81, v[120:123] offset:1024
	s_nop 0
	v_mfma_f32_32x32x16_f16 a[64:79], v[8:11], v[60:63], a[64:79]
	ds_write_b128 v81, v[124:127] offset:2048
	ds_write_b128 v81, v[128:131] offset:3072
	v_mfma_f32_32x32x16_f16 a[48:63], v[12:15], v[60:63], a[48:63]
	ds_read_b128 v[100:103], v95
	ds_read_b128 v[104:107], v96
	ds_read_b128 v[108:111], v97
	ds_read_b128 v[112:115], v94
	s_waitcnt vmcnt(10)
	s_waitcnt lgkmcnt(8)
	s_barrier
	ds_read_b128 v[4:7], v84 offset:54208
	ds_read_b128 v[8:11], v84 offset:55232
	ds_read_b128 v[12:15], v84 offset:56256
	s_nop 0
	v_mfma_f32_32x32x16_f16 a[32:47], v[16:19], v[60:63], a[32:47]
	ds_read_b128 v[16:19], v84 offset:57280
	v_mfma_f32_32x32x16_f16 a[16:31], v[20:23], v[60:63], a[16:31]
	ds_read_b128 v[20:23], v84 offset:58304
	v_mfma_f32_32x32x16_f16 a[0:15], v[24:27], v[60:63], a[0:15]
	ds_read_b128 v[24:27], v84 offset:59328
	s_waitcnt lgkmcnt(6)
	s_nop 0
	v_mfma_f32_32x32x16_f16 a[80:95], v[28:31], v[0:3], a[80:95]
	s_add_u32 m0, s46, 0x3000
	s_add_u32 s40, s40, 0x1800
	s_addc_u32 s41, s41, 0
	global_load_lds_dwordx4 v76, s[40:41]
	ds_read_b128 v[28:31], v84 offset:60352
	s_nop 0
	v_mfma_f32_32x32x16_f16 a[64:79], v[32:35], v[0:3], a[64:79]
	global_load_dwordx4 v[116:119], v64, s[4:5] offset:1440
	global_load_dwordx4 v[120:123], v66, s[4:5] offset:1440
	ds_read_b128 v[32:35], v84 offset:61376
	v_mfma_f32_32x32x16_f16 a[48:63], v[36:39], v[0:3], a[48:63]
	s_add_u32 m0, s47, 0x3000
	s_add_u32 s42, s42, 0x1800
	s_addc_u32 s43, s43, 0
	global_load_lds_dwordx4 v77, s[42:43]
	ds_read_b128 v[36:39], v84 offset:62400
	s_nop 0
	v_mfma_f32_32x32x16_f16 a[32:47], v[40:43], v[0:3], a[32:47]
	global_load_dwordx4 v[124:127], v68, s[4:5] offset:1440
	global_load_dwordx4 v[128:131], v70, s[4:5] offset:1440
	ds_read_b128 v[40:43], v84 offset:63424
	v_mfma_f32_32x32x16_f16 a[16:31], v[44:47], v[0:3], a[16:31]
	s_add_u32 m0, s48, 0x3000
	s_add_u32 s44, s44, 0x1800
	s_addc_u32 s45, s45, 0
	global_load_lds_dwordx4 v78, s[44:45]
	ds_read_b128 v[44:47], v84 offset:64448
	s_nop 0
	v_mfma_f32_32x32x16_f16 a[0:15], v[48:51], v[0:3], a[0:15]
	ds_read_b128 v[48:51], v84 offset:65472
	s_waitcnt lgkmcnt(6)
	s_nop 0
	v_mfma_f32_32x32x16_f16 a[80:95], v[4:7], v[100:103], a[80:95]
	v_mfma_f32_32x32x16_f16 a[64:79], v[8:11], v[100:103], a[64:79]
	v_mfma_f32_32x32x16_f16 a[48:63], v[12:15], v[100:103], a[48:63]
	s_waitcnt vmcnt(10)
	s_waitcnt lgkmcnt(0)
	s_barrier
	ds_read_b128 v[4:7], v98
	ds_read_b128 v[8:11], v98 offset:1024
	ds_read_b128 v[12:15], v98 offset:2048
	s_nop 0
	v_mfma_f32_32x32x16_f16 a[32:47], v[16:19], v[100:103], a[32:47]
	ds_read_b128 v[16:19], v98 offset:3072
	v_mfma_f32_32x32x16_f16 a[16:31], v[20:23], v[100:103], a[16:31]
	ds_read_b128 v[20:23], v98 offset:4096
	v_mfma_f32_32x32x16_f16 a[0:15], v[24:27], v[100:103], a[0:15]
	ds_read_b128 v[24:27], v98 offset:5120
	v_mfma_f32_32x32x16_f16 a[80:95], v[28:31], v[104:107], a[80:95]
	s_add_u32 m0, s46, 0xd3c0
	s_add_u32 s40, s40, 0x1800
	s_addc_u32 s41, s41, 0
	global_load_lds_dwordx4 v76, s[40:41]
	ds_read_b128 v[28:31], v98 offset:6144
	s_nop 0
	v_mfma_f32_32x32x16_f16 a[64:79], v[32:35], v[104:107], a[64:79]
	ds_read_b128 v[32:35], v98 offset:7168
	v_mfma_f32_32x32x16_f16 a[48:63], v[36:39], v[104:107], a[48:63]
	s_add_u32 m0, s47, 0xd3c0
	s_add_u32 s42, s42, 0x1800
	s_addc_u32 s43, s43, 0
	global_load_lds_dwordx4 v77, s[42:43]
	ds_read_b128 v[36:39], v98 offset:8192
	s_nop 0
	v_mfma_f32_32x32x16_f16 a[32:47], v[40:43], v[104:107], a[32:47]
	ds_read_b128 v[40:43], v98 offset:9216
	v_mfma_f32_32x32x16_f16 a[16:31], v[44:47], v[104:107], a[16:31]
	s_add_u32 m0, s48, 0xd3c0
	s_add_u32 s44, s44, 0x1800
	s_addc_u32 s45, s45, 0
	global_load_lds_dwordx4 v78, s[44:45]
	ds_read_b128 v[44:47], v98 offset:10240
	s_nop 0
	v_mfma_f32_32x32x16_f16 a[0:15], v[48:51], v[104:107], a[0:15]
	ds_read_b128 v[48:51], v98 offset:11264
	s_waitcnt lgkmcnt(6)
	s_nop 0
	v_mfma_f32_32x32x16_f16 a[80:95], v[4:7], v[108:111], a[80:95]
	s_waitcnt vmcnt(24)
	ds_write_b128 v81, v[132:135]
	ds_write_b128 v81, v[136:139] offset:1024
	s_nop 0
	v_mfma_f32_32x32x16_f16 a[64:79], v[8:11], v[108:111], a[64:79]
	ds_write_b128 v81, v[140:143] offset:2048
	ds_write_b128 v81, v[144:147] offset:3072
	v_mfma_f32_32x32x16_f16 a[48:63], v[12:15], v[108:111], a[48:63]
	ds_read_b128 v[52:55], v95
	ds_read_b128 v[56:59], v96
	ds_read_b128 v[60:63], v97
	ds_read_b128 v[0:3], v94
	s_waitcnt vmcnt(10)
	s_waitcnt lgkmcnt(8)
	s_barrier
	ds_read_b128 v[4:7], v84 offset:0
	ds_read_b128 v[8:11], v84 offset:1024
	ds_read_b128 v[12:15], v84 offset:2048
	s_nop 0
	v_mfma_f32_32x32x16_f16 a[32:47], v[16:19], v[108:111], a[32:47]
	ds_read_b128 v[16:19], v84 offset:3072
	v_mfma_f32_32x32x16_f16 a[16:31], v[20:23], v[108:111], a[16:31]
	ds_read_b128 v[20:23], v84 offset:4096
	v_mfma_f32_32x32x16_f16 a[0:15], v[24:27], v[108:111], a[0:15]
	ds_read_b128 v[24:27], v84 offset:5120
	s_waitcnt lgkmcnt(6)
	s_nop 0
	v_mfma_f32_32x32x16_f16 a[80:95], v[28:31], v[112:115], a[80:95]
	s_add_u32 m0, s46, 0x103c0
	s_add_u32 s40, s40, 0x1800
	s_addc_u32 s41, s41, 0
	global_load_lds_dwordx4 v76, s[40:41]
	ds_read_b128 v[28:31], v84 offset:6144
	s_nop 0
	v_mfma_f32_32x32x16_f16 a[64:79], v[32:35], v[112:115], a[64:79]
	ds_read_b128 v[32:35], v84 offset:7168
	v_mfma_f32_32x32x16_f16 a[48:63], v[36:39], v[112:115], a[48:63]
	s_add_u32 m0, s47, 0x103c0
	s_add_u32 s42, s42, 0x1800
	s_addc_u32 s43, s43, 0
	global_load_lds_dwordx4 v77, s[42:43]
	ds_read_b128 v[36:39], v84 offset:8192
	s_nop 0
	v_mfma_f32_32x32x16_f16 a[32:47], v[40:43], v[112:115], a[32:47]
	ds_read_b128 v[40:43], v84 offset:9216
	v_mfma_f32_32x32x16_f16 a[16:31], v[44:47], v[112:115], a[16:31]
	s_add_u32 m0, s48, 0x103c0
	s_add_u32 s44, s44, 0x1800
	s_addc_u32 s45, s45, 0
	global_load_lds_dwordx4 v78, s[44:45]
	ds_read_b128 v[44:47], v84 offset:10240
	s_nop 0
	v_mfma_f32_32x32x16_f16 a[0:15], v[48:51], v[112:115], a[0:15]
	ds_read_b128 v[48:51], v84 offset:11264
	s_waitcnt lgkmcnt(6)
	s_nop 0
	v_mfma_f32_32x32x16_f16 a[80:95], v[4:7], v[52:55], a[80:95]
	v_mfma_f32_32x32x16_f16 a[64:79], v[8:11], v[52:55], a[64:79]
	v_mfma_f32_32x32x16_f16 a[48:63], v[12:15], v[52:55], a[48:63]
	s_waitcnt vmcnt(6)
	s_waitcnt lgkmcnt(0)
	s_barrier
	ds_read_b128 v[4:7], v84 offset:12288
	ds_read_b128 v[8:11], v84 offset:13312
	ds_read_b128 v[12:15], v84 offset:14336
	s_nop 0
	v_mfma_f32_32x32x16_f16 a[32:47], v[16:19], v[52:55], a[32:47]
	ds_read_b128 v[16:19], v84 offset:15360
	v_mfma_f32_32x32x16_f16 a[16:31], v[20:23], v[52:55], a[16:31]
	ds_read_b128 v[20:23], v84 offset:16384
	v_mfma_f32_32x32x16_f16 a[0:15], v[24:27], v[52:55], a[0:15]
	ds_read_b128 v[24:27], v84 offset:17408
	v_mfma_f32_32x32x16_f16 a[80:95], v[28:31], v[56:59], a[80:95]
	s_add_u32 m0, s46, 0x0
	s_add_u32 s40, s40, 0x1800
	s_addc_u32 s41, s41, 0
	global_load_lds_dwordx4 v76, s[40:41]
	ds_read_b128 v[28:31], v84 offset:18432
	v_mfma_f32_32x32x16_f16 a[64:79], v[32:35], v[56:59], a[64:79]
	ds_read_b128 v[32:35], v84 offset:19456
	v_mfma_f32_32x32x16_f16 a[48:63], v[36:39], v[56:59], a[48:63]
	s_add_u32 m0, s47, 0x0
	s_add_u32 s42, s42, s49
	s_addc_u32 s43, s43, 0
	global_load_lds_dwordx4 v77, s[42:43]
	ds_read_b128 v[36:39], v84 offset:20480
	s_nop 0
	v_mfma_f32_32x32x16_f16 a[32:47], v[40:43], v[56:59], a[32:47]
	ds_read_b128 v[40:43], v84 offset:21504
	v_mfma_f32_32x32x16_f16 a[16:31], v[44:47], v[56:59], a[16:31]
	s_add_u32 m0, s48, 0x0
	s_add_u32 s44, s44, 0xc00
	s_addc_u32 s45, s45, 0
	global_load_lds_dwordx4 v78, s[44:45]
	ds_read_b128 v[44:47], v84 offset:22528
	v_mfma_f32_32x32x16_f16 a[0:15], v[48:51], v[56:59], a[0:15]
	ds_read_b128 v[48:51], v84 offset:23552
	s_waitcnt lgkmcnt(6)
	s_nop 0
	v_mfma_f32_32x32x16_f16 a[80:95], v[4:7], v[60:63], a[80:95]
	s_waitcnt vmcnt(20)
	ds_write_b128 v81, v[148:151]
	ds_write_b128 v81, v[152:155] offset:1024
	s_nop 0
	v_mfma_f32_32x32x16_f16 a[64:79], v[8:11], v[60:63], a[64:79]
	ds_write_b128 v81, v[156:159] offset:2048
	ds_write_b128 v81, v[72:75] offset:3072
	v_mfma_f32_32x32x16_f16 a[48:63], v[12:15], v[60:63], a[48:63]
	ds_read_b128 v[100:103], v95
	ds_read_b128 v[104:107], v96
	ds_read_b128 v[108:111], v97
	ds_read_b128 v[112:115], v94
	s_waitcnt vmcnt(6)
	s_waitcnt lgkmcnt(8)
	s_barrier
	ds_read_b128 v[4:7], v84 offset:54208
	ds_read_b128 v[8:11], v84 offset:55232
	ds_read_b128 v[12:15], v84 offset:56256
	s_nop 0
	v_mfma_f32_32x32x16_f16 a[32:47], v[16:19], v[60:63], a[32:47]
	ds_read_b128 v[16:19], v84 offset:57280
	v_mfma_f32_32x32x16_f16 a[16:31], v[20:23], v[60:63], a[16:31]
	ds_read_b128 v[20:23], v84 offset:58304
	v_mfma_f32_32x32x16_f16 a[0:15], v[24:27], v[60:63], a[0:15]
	ds_read_b128 v[24:27], v84 offset:59328
	s_waitcnt lgkmcnt(6)
	s_nop 0
	v_mfma_f32_32x32x16_f16 a[80:95], v[28:31], v[0:3], a[80:95]
	ds_read_b128 v[28:31], v84 offset:60352
	v_mfma_f32_32x32x16_f16 a[64:79], v[32:35], v[0:3], a[64:79]
	ds_read_b128 v[32:35], v84 offset:61376
	v_mfma_f32_32x32x16_f16 a[48:63], v[36:39], v[0:3], a[48:63]
	ds_read_b128 v[36:39], v84 offset:62400
	v_mfma_f32_32x32x16_f16 a[32:47], v[40:43], v[0:3], a[32:47]
	ds_read_b128 v[40:43], v84 offset:63424
	v_mfma_f32_32x32x16_f16 a[16:31], v[44:47], v[0:3], a[16:31]
	ds_read_b128 v[44:47], v84 offset:64448
	v_mfma_f32_32x32x16_f16 a[0:15], v[48:51], v[0:3], a[0:15]
	ds_read_b128 v[48:51], v84 offset:65472
	s_waitcnt lgkmcnt(6)
	s_nop 0
	v_mfma_f32_32x32x16_f16 a[80:95], v[4:7], v[100:103], a[80:95]
	v_mfma_f32_32x32x16_f16 a[64:79], v[8:11], v[100:103], a[64:79]
	v_mfma_f32_32x32x16_f16 a[48:63], v[12:15], v[100:103], a[48:63]
	s_waitcnt vmcnt(3)
	s_waitcnt lgkmcnt(0)
	s_barrier
	ds_read_b128 v[4:7], v98
	ds_read_b128 v[8:11], v98 offset:1024
	ds_read_b128 v[12:15], v98 offset:2048
	s_nop 0
	v_mfma_f32_32x32x16_f16 a[32:47], v[16:19], v[100:103], a[32:47]
	ds_read_b128 v[16:19], v98 offset:3072
	v_mfma_f32_32x32x16_f16 a[16:31], v[20:23], v[100:103], a[16:31]
	ds_read_b128 v[20:23], v98 offset:4096
	v_mfma_f32_32x32x16_f16 a[0:15], v[24:27], v[100:103], a[0:15]
	ds_read_b128 v[24:27], v98 offset:5120
	v_mfma_f32_32x32x16_f16 a[80:95], v[28:31], v[104:107], a[80:95]
	ds_read_b128 v[28:31], v98 offset:6144
	v_mfma_f32_32x32x16_f16 a[64:79], v[32:35], v[104:107], a[64:79]
	ds_read_b128 v[32:35], v98 offset:7168
	v_mfma_f32_32x32x16_f16 a[48:63], v[36:39], v[104:107], a[48:63]
	ds_read_b128 v[36:39], v98 offset:8192
	v_mfma_f32_32x32x16_f16 a[32:47], v[40:43], v[104:107], a[32:47]
	ds_read_b128 v[40:43], v98 offset:9216
	v_mfma_f32_32x32x16_f16 a[16:31], v[44:47], v[104:107], a[16:31]
	ds_read_b128 v[44:47], v98 offset:10240
	v_mfma_f32_32x32x16_f16 a[0:15], v[48:51], v[104:107], a[0:15]
	ds_read_b128 v[48:51], v98 offset:11264
	s_waitcnt lgkmcnt(6)
	s_nop 0
	v_mfma_f32_32x32x16_f16 a[80:95], v[4:7], v[108:111], a[80:95]
	s_waitcnt vmcnt(10)
	ds_write_b128 v81, v[116:119]
	ds_write_b128 v81, v[120:123] offset:1024
	s_nop 0
	v_mfma_f32_32x32x16_f16 a[64:79], v[8:11], v[108:111], a[64:79]
	ds_write_b128 v81, v[124:127] offset:2048
	ds_write_b128 v81, v[128:131] offset:3072
	v_mfma_f32_32x32x16_f16 a[48:63], v[12:15], v[108:111], a[48:63]
	ds_read_b128 v[0:3], v94
	s_waitcnt vmcnt(0)
	s_waitcnt lgkmcnt(5)
	s_barrier
	ds_read_b128 v[4:7], v84 offset:0
	ds_read_b128 v[8:11], v84 offset:1024
	ds_read_b128 v[12:15], v84 offset:2048
	s_nop 0
	v_mfma_f32_32x32x16_f16 a[32:47], v[16:19], v[108:111], a[32:47]
	ds_read_b128 v[16:19], v84 offset:3072
	v_mfma_f32_32x32x16_f16 a[16:31], v[20:23], v[108:111], a[16:31]
	ds_read_b128 v[20:23], v84 offset:4096
	v_mfma_f32_32x32x16_f16 a[0:15], v[24:27], v[108:111], a[0:15]
	ds_read_b128 v[24:27], v84 offset:5120
	s_waitcnt lgkmcnt(6)
	s_nop 0
	v_mfma_f32_32x32x16_f16 a[80:95], v[28:31], v[112:115], a[80:95]
	v_mfma_f32_32x32x16_f16 a[64:79], v[32:35], v[112:115], a[64:79]
	v_mfma_f32_32x32x16_f16 a[48:63], v[36:39], v[112:115], a[48:63]
	v_mfma_f32_32x32x16_f16 a[32:47], v[40:43], v[112:115], a[32:47]
	v_mfma_f32_32x32x16_f16 a[16:31], v[44:47], v[112:115], a[16:31]
	v_mfma_f32_32x32x16_f16 a[0:15], v[48:51], v[112:115], a[0:15]
	s_waitcnt lgkmcnt(0)
	v_mfma_f32_32x32x16_f16 a[80:95], v[4:7], v[0:3], a[80:95]
	v_mfma_f32_32x32x16_f16 a[16:31], v[20:23], v[0:3], a[16:31]
	v_lshlrev_b32_e32 v22, 4, v85
	v_mfma_f32_32x32x16_f16 a[64:79], v[8:11], v[0:3], a[64:79]
	v_mfma_f32_32x32x16_f16 a[48:63], v[12:15], v[0:3], a[48:63]
	s_nop 7
	v_accvgpr_read_b32 v13, a88
	v_mfma_f32_32x32x16_f16 a[32:47], v[16:19], v[0:3], a[32:47]
	v_accvgpr_read_b32 v17, a92
	v_mfma_f32_32x32x16_f16 a[0:15], v[24:27], v[0:3], a[0:15]
	ds_read_b128 v[2:5], v22 offset:53248
	ds_read_b128 v[6:9], v22 offset:53280
	v_accvgpr_read_b32 v1, a80
	v_lshlrev_b32_e32 v0, 4, v92
	s_waitcnt lgkmcnt(1)
	v_add_f32_e32 v1, v1, v2
	v_accvgpr_read_b32 v2, a81
	v_add_f32_e32 v2, v3, v2
	v_max_f32_e32 v10, 0, v2
	v_accvgpr_read_b32 v2, a82
	v_add_f32_e32 v2, v4, v2
	v_max_f32_e32 v11, 0, v2
	v_accvgpr_read_b32 v2, a83
	v_add_f32_e32 v2, v5, v2
	v_max_f32_e32 v12, 0, v2
	v_accvgpr_read_b32 v2, a84
	s_waitcnt lgkmcnt(0)
	v_add_f32_e32 v2, v2, v6
	v_max_f32_e32 v6, 0, v2
	v_accvgpr_read_b32 v2, a85
	v_add_f32_e32 v2, v7, v2
	v_max_f32_e32 v7, 0, v2
	v_accvgpr_read_b32 v2, a86
	v_add_f32_e32 v2, v8, v2
	v_max_f32_e32 v8, 0, v2
	v_accvgpr_read_b32 v2, a87
	v_add_f32_e32 v2, v9, v2
	v_max_f32_e32 v9, 0, v2
	ds_read_b128 v[2:5], v22 offset:53312
	v_max_f32_e32 v1, 0, v1
	s_waitcnt lgkmcnt(0)
	v_add_f32_e32 v2, v13, v2
	v_max_f32_e32 v13, 0, v2
	v_accvgpr_read_b32 v2, a89
	v_add_f32_e32 v2, v3, v2
	v_max_f32_e32 v14, 0, v2
	v_accvgpr_read_b32 v2, a90
	v_add_f32_e32 v2, v4, v2
	v_max_f32_e32 v15, 0, v2
	v_accvgpr_read_b32 v2, a91
	v_add_f32_e32 v2, v5, v2
	v_max_f32_e32 v16, 0, v2
	ds_read_b128 v[2:5], v22 offset:53344
	s_waitcnt lgkmcnt(0)
	v_add_f32_e32 v2, v17, v2
	v_max_f32_e32 v17, 0, v2
	v_accvgpr_read_b32 v2, a93
	v_add_f32_e32 v2, v3, v2
	v_max_f32_e32 v18, 0, v2
	v_accvgpr_read_b32 v2, a94
	v_add_f32_e32 v2, v4, v2
	v_max_f32_e32 v19, 0, v2
	v_accvgpr_read_b32 v2, a95
	v_add_f32_e32 v2, v5, v2
	v_cvt_pk_f16_f32 v5, v8, v9
	v_cvt_pk_f16_f32 v4, v6, v7
	ds_read_b128 v[6:9], v0 offset:40960
	v_max_f32_e32 v20, 0, v2
	v_cvt_pk_f16_f32 v3, v11, v12
	v_cvt_pk_f16_f32 v2, v1, v10
	v_accvgpr_read_b32 v1, a64
	s_waitcnt lgkmcnt(0)
	v_mfma_f32_32x32x16_f16 a[80:95], v[6:9], v[2:5], 0
	ds_read_b128 v[6:9], v0 offset:41984
	v_cvt_pk_f16_f32 v5, v19, v20
	v_cvt_pk_f16_f32 v4, v17, v18
	v_cvt_pk_f16_f32 v3, v15, v16
	v_cvt_pk_f16_f32 v2, v13, v14
	v_accvgpr_read_b32 v13, a72
	v_accvgpr_read_b32 v17, a76
	s_waitcnt lgkmcnt(0)
	v_mfma_f32_32x32x16_f16 a[80:95], v[6:9], v[2:5], a[80:95]
	ds_read_b128 v[2:5], v22 offset:53376
	v_accvgpr_read_b32 v9, a68
	s_waitcnt lgkmcnt(0)
	v_add_f32_e32 v1, v1, v2
	v_accvgpr_read_b32 v2, a65
	v_add_f32_e32 v2, v3, v2
	v_max_f32_e32 v6, 0, v2
	v_accvgpr_read_b32 v2, a66
	v_add_f32_e32 v2, v4, v2
	v_max_f32_e32 v7, 0, v2
	v_accvgpr_read_b32 v2, a67
	v_add_f32_e32 v2, v5, v2
	v_max_f32_e32 v8, 0, v2
	ds_read_b128 v[2:5], v22 offset:53408
	v_max_f32_e32 v1, 0, v1
	s_waitcnt lgkmcnt(0)
	v_add_f32_e32 v2, v9, v2
	v_max_f32_e32 v9, 0, v2
	v_accvgpr_read_b32 v2, a69
	v_add_f32_e32 v2, v3, v2
	v_max_f32_e32 v10, 0, v2
	v_accvgpr_read_b32 v2, a70
	v_add_f32_e32 v2, v4, v2
	v_max_f32_e32 v11, 0, v2
	v_accvgpr_read_b32 v2, a71
	v_add_f32_e32 v2, v5, v2
	v_max_f32_e32 v12, 0, v2
	ds_read_b128 v[2:5], v22 offset:53440
	s_waitcnt lgkmcnt(0)
	v_add_f32_e32 v2, v13, v2
	v_max_f32_e32 v13, 0, v2
	v_accvgpr_read_b32 v2, a73
	v_add_f32_e32 v2, v3, v2
	v_max_f32_e32 v14, 0, v2
	v_accvgpr_read_b32 v2, a74
	v_add_f32_e32 v2, v4, v2
	v_max_f32_e32 v15, 0, v2
	v_accvgpr_read_b32 v2, a75
	v_add_f32_e32 v2, v5, v2
	v_max_f32_e32 v16, 0, v2
	ds_read_b128 v[2:5], v22 offset:53472
	s_waitcnt lgkmcnt(0)
	v_add_f32_e32 v2, v17, v2
	v_max_f32_e32 v17, 0, v2
	v_accvgpr_read_b32 v2, a77
	v_add_f32_e32 v2, v3, v2
	v_max_f32_e32 v18, 0, v2
	v_accvgpr_read_b32 v2, a78
	v_add_f32_e32 v2, v4, v2
	v_max_f32_e32 v19, 0, v2
	v_accvgpr_read_b32 v2, a79
	v_add_f32_e32 v2, v5, v2
	v_max_f32_e32 v20, 0, v2
	v_cvt_pk_f16_f32 v4, v9, v10
	v_cvt_pk_f16_f32 v3, v7, v8
	v_cvt_pk_f16_f32 v2, v1, v6
	ds_read_b128 v[6:9], v0 offset:43008
	v_cvt_pk_f16_f32 v5, v11, v12
	v_accvgpr_read_b32 v1, a48
	s_waitcnt lgkmcnt(0)
	v_mfma_f32_32x32x16_f16 a[80:95], v[6:9], v[2:5], a[80:95]
	ds_read_b128 v[6:9], v0 offset:44032
	v_cvt_pk_f16_f32 v5, v19, v20
	v_cvt_pk_f16_f32 v4, v17, v18
	v_cvt_pk_f16_f32 v3, v15, v16
	v_cvt_pk_f16_f32 v2, v13, v14
	v_accvgpr_read_b32 v13, a56
	v_accvgpr_read_b32 v17, a60
	s_waitcnt lgkmcnt(0)
	v_mfma_f32_32x32x16_f16 a[80:95], v[6:9], v[2:5], a[80:95]
	ds_read_b128 v[2:5], v22 offset:53504
	v_accvgpr_read_b32 v9, a52
	s_waitcnt lgkmcnt(0)
	v_add_f32_e32 v1, v1, v2
	v_accvgpr_read_b32 v2, a49
	v_add_f32_e32 v2, v3, v2
	v_max_f32_e32 v6, 0, v2
	v_accvgpr_read_b32 v2, a50
	v_add_f32_e32 v2, v4, v2
	v_max_f32_e32 v7, 0, v2
	v_accvgpr_read_b32 v2, a51
	v_add_f32_e32 v2, v5, v2
	v_max_f32_e32 v8, 0, v2
	ds_read_b128 v[2:5], v22 offset:53536
	v_max_f32_e32 v1, 0, v1
	s_waitcnt lgkmcnt(0)
	v_add_f32_e32 v2, v9, v2
	v_max_f32_e32 v9, 0, v2
	v_accvgpr_read_b32 v2, a53
	v_add_f32_e32 v2, v3, v2
	v_max_f32_e32 v10, 0, v2
	v_accvgpr_read_b32 v2, a54
	v_add_f32_e32 v2, v4, v2
	v_max_f32_e32 v11, 0, v2
	v_accvgpr_read_b32 v2, a55
	v_add_f32_e32 v2, v5, v2
	v_max_f32_e32 v12, 0, v2
	ds_read_b128 v[2:5], v22 offset:53568
	s_waitcnt lgkmcnt(0)
	v_add_f32_e32 v2, v13, v2
	v_max_f32_e32 v13, 0, v2
	v_accvgpr_read_b32 v2, a57
	v_add_f32_e32 v2, v3, v2
	v_max_f32_e32 v14, 0, v2
	v_accvgpr_read_b32 v2, a58
	v_add_f32_e32 v2, v4, v2
	v_max_f32_e32 v15, 0, v2
	v_accvgpr_read_b32 v2, a59
	v_add_f32_e32 v2, v5, v2
	v_max_f32_e32 v16, 0, v2
	ds_read_b128 v[2:5], v22 offset:53600
	s_waitcnt lgkmcnt(0)
	v_add_f32_e32 v2, v17, v2
	v_max_f32_e32 v17, 0, v2
	v_accvgpr_read_b32 v2, a61
	v_add_f32_e32 v2, v3, v2
	v_max_f32_e32 v18, 0, v2
	v_accvgpr_read_b32 v2, a62
	v_add_f32_e32 v2, v4, v2
	v_max_f32_e32 v19, 0, v2
	v_accvgpr_read_b32 v2, a63
	v_add_f32_e32 v2, v5, v2
	v_max_f32_e32 v20, 0, v2
	v_cvt_pk_f16_f32 v4, v9, v10
	v_cvt_pk_f16_f32 v3, v7, v8
	v_cvt_pk_f16_f32 v2, v1, v6
	ds_read_b128 v[6:9], v0 offset:45056
	v_cvt_pk_f16_f32 v5, v11, v12
	v_accvgpr_read_b32 v1, a32
	s_waitcnt lgkmcnt(0)
	v_mfma_f32_32x32x16_f16 a[80:95], v[6:9], v[2:5], a[80:95]
	ds_read_b128 v[6:9], v0 offset:46080
	v_cvt_pk_f16_f32 v5, v19, v20
	v_cvt_pk_f16_f32 v4, v17, v18
	v_cvt_pk_f16_f32 v3, v15, v16
	v_cvt_pk_f16_f32 v2, v13, v14
	v_accvgpr_read_b32 v13, a40
	v_accvgpr_read_b32 v17, a44
	s_waitcnt lgkmcnt(0)
	v_mfma_f32_32x32x16_f16 a[80:95], v[6:9], v[2:5], a[80:95]
	ds_read_b128 v[2:5], v22 offset:53632
	v_accvgpr_read_b32 v9, a36
	s_waitcnt lgkmcnt(0)
	v_add_f32_e32 v1, v1, v2
	v_accvgpr_read_b32 v2, a33
	v_add_f32_e32 v2, v3, v2
	v_max_f32_e32 v6, 0, v2
	v_accvgpr_read_b32 v2, a34
	v_add_f32_e32 v2, v4, v2
	v_max_f32_e32 v7, 0, v2
	v_accvgpr_read_b32 v2, a35
	v_add_f32_e32 v2, v5, v2
	v_max_f32_e32 v8, 0, v2
	ds_read_b128 v[2:5], v22 offset:53664
	v_max_f32_e32 v1, 0, v1
	s_waitcnt lgkmcnt(0)
	v_add_f32_e32 v2, v9, v2
	v_max_f32_e32 v9, 0, v2
	v_accvgpr_read_b32 v2, a37
	v_add_f32_e32 v2, v3, v2
	v_max_f32_e32 v10, 0, v2
	v_accvgpr_read_b32 v2, a38
	v_add_f32_e32 v2, v4, v2
	v_max_f32_e32 v11, 0, v2
	v_accvgpr_read_b32 v2, a39
	v_add_f32_e32 v2, v5, v2
	v_max_f32_e32 v12, 0, v2
	ds_read_b128 v[2:5], v22 offset:53696
	s_waitcnt lgkmcnt(0)
	v_add_f32_e32 v2, v13, v2
	v_max_f32_e32 v13, 0, v2
	v_accvgpr_read_b32 v2, a41
	v_add_f32_e32 v2, v3, v2
	v_max_f32_e32 v14, 0, v2
	v_accvgpr_read_b32 v2, a42
	v_add_f32_e32 v2, v4, v2
	v_max_f32_e32 v15, 0, v2
	v_accvgpr_read_b32 v2, a43
	v_add_f32_e32 v2, v5, v2
	v_max_f32_e32 v16, 0, v2
	ds_read_b128 v[2:5], v22 offset:53728
	s_waitcnt lgkmcnt(0)
	v_add_f32_e32 v2, v17, v2
	v_max_f32_e32 v17, 0, v2
	v_accvgpr_read_b32 v2, a45
	v_add_f32_e32 v2, v3, v2
	v_max_f32_e32 v18, 0, v2
	v_accvgpr_read_b32 v2, a46
	v_add_f32_e32 v2, v4, v2
	v_max_f32_e32 v19, 0, v2
	v_accvgpr_read_b32 v2, a47
	v_add_f32_e32 v2, v5, v2
	v_max_f32_e32 v20, 0, v2
	v_cvt_pk_f16_f32 v4, v9, v10
	v_cvt_pk_f16_f32 v3, v7, v8
	v_cvt_pk_f16_f32 v2, v1, v6
	ds_read_b128 v[6:9], v0 offset:47104
	v_cvt_pk_f16_f32 v5, v11, v12
	v_accvgpr_read_b32 v1, a16
	s_waitcnt lgkmcnt(0)
	v_mfma_f32_32x32x16_f16 a[32:47], v[6:9], v[2:5], 0
	ds_read_b128 v[6:9], v0 offset:48128
	v_cvt_pk_f16_f32 v5, v19, v20
	v_cvt_pk_f16_f32 v4, v17, v18
	v_cvt_pk_f16_f32 v3, v15, v16
	v_cvt_pk_f16_f32 v2, v13, v14
	v_accvgpr_read_b32 v13, a24
	v_accvgpr_read_b32 v17, a28
	s_waitcnt lgkmcnt(0)
	v_mfma_f32_32x32x16_f16 a[32:47], v[6:9], v[2:5], a[32:47]
	ds_read_b128 v[2:5], v22 offset:53760
	v_accvgpr_read_b32 v9, a20
	s_waitcnt lgkmcnt(0)
	v_add_f32_e32 v1, v1, v2
	v_accvgpr_read_b32 v2, a17
	v_add_f32_e32 v2, v3, v2
	v_max_f32_e32 v6, 0, v2
	v_accvgpr_read_b32 v2, a18
	v_add_f32_e32 v2, v4, v2
	v_max_f32_e32 v7, 0, v2
	v_accvgpr_read_b32 v2, a19
	v_add_f32_e32 v2, v5, v2
	v_max_f32_e32 v8, 0, v2
	ds_read_b128 v[2:5], v22 offset:53792
	v_max_f32_e32 v1, 0, v1
	s_waitcnt lgkmcnt(0)
	v_add_f32_e32 v2, v9, v2
	v_max_f32_e32 v9, 0, v2
	v_accvgpr_read_b32 v2, a21
	v_add_f32_e32 v2, v3, v2
	v_max_f32_e32 v10, 0, v2
	v_accvgpr_read_b32 v2, a22
	v_add_f32_e32 v2, v4, v2
	v_max_f32_e32 v11, 0, v2
	v_accvgpr_read_b32 v2, a23
	v_add_f32_e32 v2, v5, v2
	v_max_f32_e32 v12, 0, v2
	ds_read_b128 v[2:5], v22 offset:53824
	s_waitcnt lgkmcnt(0)
	v_add_f32_e32 v2, v13, v2
	v_max_f32_e32 v13, 0, v2
	v_accvgpr_read_b32 v2, a25
	v_add_f32_e32 v2, v3, v2
	v_max_f32_e32 v14, 0, v2
	v_accvgpr_read_b32 v2, a26
	v_add_f32_e32 v2, v4, v2
	v_max_f32_e32 v15, 0, v2
	v_accvgpr_read_b32 v2, a27
	v_add_f32_e32 v2, v5, v2
	v_max_f32_e32 v16, 0, v2
	ds_read_b128 v[2:5], v22 offset:53856
	s_waitcnt lgkmcnt(0)
	v_add_f32_e32 v2, v17, v2
	v_max_f32_e32 v17, 0, v2
	v_accvgpr_read_b32 v2, a29
	v_add_f32_e32 v2, v3, v2
	v_max_f32_e32 v18, 0, v2
	v_accvgpr_read_b32 v2, a30
	v_add_f32_e32 v2, v4, v2
	v_max_f32_e32 v19, 0, v2
	v_accvgpr_read_b32 v2, a31
	v_add_f32_e32 v2, v5, v2
	v_max_f32_e32 v20, 0, v2
	v_cvt_pk_f16_f32 v4, v9, v10
	v_cvt_pk_f16_f32 v3, v7, v8
	v_cvt_pk_f16_f32 v2, v1, v6
	ds_read_b128 v[6:9], v0 offset:49152
	v_cvt_pk_f16_f32 v5, v11, v12
	v_accvgpr_read_b32 v1, a0
	s_waitcnt lgkmcnt(0)
	v_mfma_f32_32x32x16_f16 a[32:47], v[6:9], v[2:5], a[32:47]
	ds_read_b128 v[6:9], v0 offset:50176
	v_cvt_pk_f16_f32 v5, v19, v20
	v_cvt_pk_f16_f32 v4, v17, v18
	v_cvt_pk_f16_f32 v3, v15, v16
	v_cvt_pk_f16_f32 v2, v13, v14
	v_accvgpr_read_b32 v13, a8
	v_accvgpr_read_b32 v17, a12
	s_waitcnt lgkmcnt(0)
	v_mfma_f32_32x32x16_f16 a[32:47], v[6:9], v[2:5], a[32:47]
	ds_read_b128 v[2:5], v22 offset:53888
	v_accvgpr_read_b32 v9, a4
	s_waitcnt lgkmcnt(0)
	v_add_f32_e32 v1, v1, v2
	v_accvgpr_read_b32 v2, a1
	v_add_f32_e32 v2, v3, v2
	v_max_f32_e32 v6, 0, v2
	v_accvgpr_read_b32 v2, a2
	v_add_f32_e32 v2, v4, v2
	v_max_f32_e32 v7, 0, v2
	v_accvgpr_read_b32 v2, a3
	v_add_f32_e32 v2, v5, v2
	v_max_f32_e32 v8, 0, v2
	ds_read_b128 v[2:5], v22 offset:53920
	v_max_f32_e32 v1, 0, v1
	s_waitcnt lgkmcnt(0)
	v_add_f32_e32 v2, v9, v2
	v_max_f32_e32 v9, 0, v2
	v_accvgpr_read_b32 v2, a5
	v_add_f32_e32 v2, v3, v2
	v_max_f32_e32 v10, 0, v2
	v_accvgpr_read_b32 v2, a6
	v_add_f32_e32 v2, v4, v2
	v_max_f32_e32 v11, 0, v2
	v_accvgpr_read_b32 v2, a7
	v_add_f32_e32 v2, v5, v2
	v_max_f32_e32 v12, 0, v2
	ds_read_b128 v[2:5], v22 offset:53952
	s_waitcnt lgkmcnt(0)
	v_add_f32_e32 v2, v13, v2
	v_max_f32_e32 v13, 0, v2
	v_accvgpr_read_b32 v2, a9
	v_add_f32_e32 v2, v3, v2
	v_max_f32_e32 v14, 0, v2
	v_accvgpr_read_b32 v2, a10
	v_add_f32_e32 v2, v4, v2
	v_max_f32_e32 v15, 0, v2
	v_accvgpr_read_b32 v2, a11
	v_add_f32_e32 v2, v5, v2
	v_max_f32_e32 v16, 0, v2
	ds_read_b128 v[2:5], v22 offset:53984
	s_waitcnt lgkmcnt(0)
	v_add_f32_e32 v2, v17, v2
	v_max_f32_e32 v17, 0, v2
	v_accvgpr_read_b32 v2, a13
	v_add_f32_e32 v2, v3, v2
	v_max_f32_e32 v18, 0, v2
	v_accvgpr_read_b32 v2, a14
	v_add_f32_e32 v2, v4, v2
	v_max_f32_e32 v19, 0, v2
	v_accvgpr_read_b32 v2, a15
	v_add_f32_e32 v2, v5, v2
	v_max_f32_e32 v20, 0, v2
	v_cvt_pk_f16_f32 v4, v9, v10
	v_cvt_pk_f16_f32 v3, v7, v8
	v_cvt_pk_f16_f32 v2, v1, v6
	ds_read_b128 v[6:9], v0 offset:51200
	v_cvt_pk_f16_f32 v5, v11, v12
	s_waitcnt lgkmcnt(0)
	s_nop 0
	v_mfma_f32_32x32x16_f16 a[32:47], v[6:9], v[2:5], a[32:47]
	ds_read_b128 v[6:9], v0 offset:52224
	v_cvt_pk_f16_f32 v5, v19, v20
	v_cvt_pk_f16_f32 v4, v17, v18
	v_cvt_pk_f16_f32 v3, v15, v16
	v_cvt_pk_f16_f32 v2, v13, v14
	s_waitcnt lgkmcnt(0)
	s_nop 0
	v_mfma_f32_32x32x16_f16 a[32:47], v[6:9], v[2:5], a[32:47]
	s_and_saveexec_b64 s[2:3], s[0:1]
	s_cbranch_execz .LBB3_39
	v_accvgpr_read_b32 v0, a80
	v_accvgpr_read_b32 v6, a86
	v_accvgpr_read_b32 v7, a87
	v_accvgpr_read_b32 v8, a88
	v_accvgpr_read_b32 v9, a89
	v_accvgpr_read_b32 v10, a90
	v_accvgpr_read_b32 v11, a91
	v_accvgpr_read_b32 v12, a92
	v_accvgpr_read_b32 v13, a93
	v_accvgpr_read_b32 v14, a94
	v_accvgpr_read_b32 v15, a95
	v_accvgpr_read_b32 v6, a32
	v_accvgpr_read_b32 v14, a40
	v_accvgpr_read_b32 v15, a41
	v_accvgpr_read_b32 v16, a42
	v_accvgpr_read_b32 v17, a43
	v_accvgpr_read_b32 v18, a44
	v_accvgpr_read_b32 v19, a45
	v_accvgpr_read_b32 v20, a46
	v_accvgpr_read_b32 v21, a47
	ds_read_b128 v[14:17], v22 offset:54016
	ds_read_b128 v[18:21], v22 offset:54080
	v_accvgpr_read_b32 v12, a38
	v_accvgpr_read_b32 v13, a39
	v_lshlrev_b32_e32 v24, 2, v85
	v_accvgpr_read_b32 v1, a81
	v_accvgpr_read_b32 v7, a33
	v_mad_i64_i32 v[12:13], s[0:1], v80, 40, s[18:19]
	v_ashrrev_i32_e32 v25, 31, v24
	v_accvgpr_read_b32 v3, a83
	v_accvgpr_read_b32 v9, a35
	v_lshl_add_u64 v[22:23], v[24:25], 2, v[12:13]
	v_mov_b32_e32 v25, v1
	s_waitcnt lgkmcnt(1)
	v_mov_b32_e32 v27, v15
	v_mov_b32_e32 v1, v7
	s_waitcnt lgkmcnt(0)
	v_mov_b32_e32 v15, v19
	v_accvgpr_read_b32 v2, a82
	v_accvgpr_read_b32 v8, a34
	v_pk_add_f32 v[0:1], v[0:1], v[14:15]
	v_mov_b32_e32 v7, v3
	v_mov_b32_e32 v15, v17
	v_mov_b32_e32 v3, v9
	v_mov_b32_e32 v17, v21
	v_mov_b32_e32 v24, v6
	v_mov_b32_e32 v26, v18
	v_mov_b32_e32 v6, v8
	v_mov_b32_e32 v14, v20
	v_pk_add_f32 v[2:3], v[2:3], v[16:17]
	v_pk_add_f32 v[24:25], v[24:25], v[26:27]
	s_waitcnt vmcnt(0)
	v_pk_mul_f32 v[0:1], v[82:83], v[0:1]
	v_pk_add_f32 v[6:7], v[6:7], v[14:15]
	v_pk_mul_f32 v[2:3], v[82:83], v[2:3]
	v_accvgpr_read_b32 v4, a84
	v_accvgpr_read_b32 v5, a85
	v_accvgpr_read_b32 v10, a36
	v_accvgpr_read_b32 v11, a37
	v_pk_fma_f32 v[0:1], v[82:83], v[24:25], v[0:1] op_sel:[1,0,0] op_sel_hi:[0,1,1]
	v_pk_fma_f32 v[2:3], v[82:83], v[6:7], v[2:3] op_sel:[1,0,0] op_sel_hi:[0,1,1]
	v_cmp_eq_u32_e32 vcc, 0, v85
	global_store_dwordx4 v[22:23], v[0:3], off
	s_and_b64 exec, exec, vcc
	s_cbranch_execz .LBB3_39
	s_mov_b32 s0, 0xd000
	v_add_u32_e64 v0, s0, 0
	ds_read2_b64 v[0:3], v0 offset0:100 offset1:108
	v_mov_b32_e32 v9, v5
	v_mov_b32_e32 v5, v11
	v_mov_b32_e32 v8, v10
	v_pk_mov_b32 v[6:7], v[82:83], v[82:83] op_sel:[1,0]
	s_waitcnt lgkmcnt(0)
	v_mov_b32_e32 v15, v1
	v_mov_b32_e32 v1, v3
	v_mov_b32_e32 v14, v2
	v_pk_add_f32 v[0:1], v[4:5], v[0:1]
	v_pk_add_f32 v[8:9], v[8:9], v[14:15]
	v_pk_mul_f32 v[0:1], v[82:83], v[0:1]
	s_nop 0
	v_pk_fma_f32 v[0:1], v[6:7], v[8:9], v[0:1]
	global_store_dwordx2 v[12:13], v[0:1], off offset:32
